# weight-prep conversions 8 chunks per round trip; PEER U: packed-mask diagonal extraction, 3-accumulator rotation, single-DPP row sums, packed gelu pair with scalar range test; PEER V: mid-token prefet
# speedup vs baseline: 1.0126x; 1.0126x over previous
; __device__ __forceinline__ void prep_phase(Frame& F, const Args& a, int layer, int blk, int nblk_, int part) {
;     ...
;         for (int it = gw; it < ntot; it += NGW) {
;             int r = it;
;             if (r < n2) { cvt8_chunk(ut, (unsigned char*)(db + DB_U), r, lane, 256.f); continue; } r -= n2;
;             if (r < n2) { cvt8_chunk(vt, (unsigned char*)(db + DB_V), r, lane, 64.f); continue; } r -= n2;
.LBB0_1194:
	v_readlane_b32 vcc_lo, v254, 44
	s_cmp_lg_u32 vcc_lo, 0x400
	s_cbranch_scc1 .Lcv_2_orig
; __device__ __forceinline__ void cvt8_chunk(const float* src, unsigned char* dst, size_t chunk, int lane, float sc) {
;     const f32x4* s = (const f32x4*)(src + chunk * 512) + lane * 2; const f32x4 a = s[0] * sc, b = s[1] * sc;
;     int w0 = 0, w1 = 0;
;     w0 = __builtin_amdgcn_cvt_pk_fp8_f32(a.x, a.y, w0, false); w0 = __builtin_amdgcn_cvt_pk_fp8_f32(a.z, a.w, w0, true);
;     w1 = __builtin_amdgcn_cvt_pk_fp8_f32(b.x, b.y, w1, false); w1 = __builtin_amdgcn_cvt_pk_fp8_f32(b.z, b.w, w1, true);
;     *(v2u*)(dst + chunk * 512 + lane * 8) = (v2u){(unsigned)w0, (unsigned)w1};
; }
; __device__ __forceinline__ void prep_phase(Frame& F, const Args& a, int layer, int blk, int nblk_, int part) {
;     ...
;         for (int it = gw; it < ntot; it += NGW) {
;             int r = it;
;             if (r < n2) { cvt8_chunk(ut, (unsigned char*)(db + DB_U), r, lane, 256.f); continue; } r -= n2;
;             if (r < n2) { cvt8_chunk(vt, (unsigned char*)(db + DB_V), r, lane, 64.f); continue; } r -= n2;
	v_lshl_add_u64 v[6:7], v[2:3], 4, s[36:37]
	s_lshl_b64 s[36:37], s[22:23], 9
	s_lshl_b64 s[22:23], s[22:23], 11
	v_lshl_add_u64 v[180:181], v[6:7], 0, s[22:23]
	v_lshl_add_u64 v[14:15], v[4:5], 0, s[38:39]
	global_load_dwordx4 v[104:107], v[180:181], off offset:16
	global_load_dwordx4 v[100:103], v[180:181], off
	v_add_co_u32_e32 v180, vcc, 0x200000, v180
	s_nop 1
	v_addc_co_u32_e32 v181, vcc, 0, v181, vcc
	global_load_dwordx4 v[112:115], v[180:181], off offset:16
	global_load_dwordx4 v[108:111], v[180:181], off
	v_add_co_u32_e32 v180, vcc, 0x200000, v180
	s_nop 1
	v_addc_co_u32_e32 v181, vcc, 0, v181, vcc
	global_load_dwordx4 v[120:123], v[180:181], off offset:16
	global_load_dwordx4 v[116:119], v[180:181], off
	v_add_co_u32_e32 v180, vcc, 0x200000, v180
	s_nop 1
	v_addc_co_u32_e32 v181, vcc, 0, v181, vcc
	global_load_dwordx4 v[128:131], v[180:181], off offset:16
	global_load_dwordx4 v[124:127], v[180:181], off
	v_add_co_u32_e32 v180, vcc, 0x200000, v180
	s_nop 1
	v_addc_co_u32_e32 v181, vcc, 0, v181, vcc
	global_load_dwordx4 v[136:139], v[180:181], off offset:16
	global_load_dwordx4 v[132:135], v[180:181], off
	v_add_co_u32_e32 v180, vcc, 0x200000, v180
	s_nop 1
	v_addc_co_u32_e32 v181, vcc, 0, v181, vcc
	global_load_dwordx4 v[144:147], v[180:181], off offset:16
	global_load_dwordx4 v[140:143], v[180:181], off
	v_add_co_u32_e32 v180, vcc, 0x200000, v180
	s_nop 1
	v_addc_co_u32_e32 v181, vcc, 0, v181, vcc
	global_load_dwordx4 v[152:155], v[180:181], off offset:16
	global_load_dwordx4 v[148:151], v[180:181], off
	v_add_co_u32_e32 v180, vcc, 0x200000, v180
	s_nop 1
	v_addc_co_u32_e32 v181, vcc, 0, v181, vcc
	global_load_dwordx4 v[160:163], v[180:181], off offset:16
	global_load_dwordx4 v[156:159], v[180:181], off
	v_lshl_add_u64 v[182:183], v[14:15], 0, s[36:37]
	s_waitcnt vmcnt(14)
	v_mov_b32_e32 v164, v0
	v_mov_b32_e32 v165, v0
	v_pk_mul_f32 v[104:105], v[104:105], s[20:21] op_sel_hi:[1,0]
	v_pk_mul_f32 v[100:101], v[100:101], s[20:21] op_sel_hi:[1,0]
	v_cvt_pk_fp8_f32 v165, v104, v105
	v_cvt_pk_fp8_f32 v164, v100, v101
	v_pk_mul_f32 v[102:103], v[102:103], s[20:21] op_sel_hi:[1,0]
	v_pk_mul_f32 v[106:107], v[106:107], s[20:21] op_sel_hi:[1,0]
	v_cvt_pk_fp8_f32 v164, v102, v103 op_sel:[0,0,1]
	v_cvt_pk_fp8_f32 v165, v106, v107 op_sel:[0,0,1]
	global_store_dwordx2 v[182:183], v[164:165], off
	s_waitcnt vmcnt(13)
	v_mov_b32_e32 v166, v0
	v_mov_b32_e32 v167, v0
	v_pk_mul_f32 v[112:113], v[112:113], s[20:21] op_sel_hi:[1,0]
	v_pk_mul_f32 v[108:109], v[108:109], s[20:21] op_sel_hi:[1,0]
	v_cvt_pk_fp8_f32 v167, v112, v113
	v_cvt_pk_fp8_f32 v166, v108, v109
	v_pk_mul_f32 v[110:111], v[110:111], s[20:21] op_sel_hi:[1,0]
	v_pk_mul_f32 v[114:115], v[114:115], s[20:21] op_sel_hi:[1,0]
	v_cvt_pk_fp8_f32 v166, v110, v111 op_sel:[0,0,1]
	v_cvt_pk_fp8_f32 v167, v114, v115 op_sel:[0,0,1]
	v_add_co_u32_e32 v182, vcc, 0x80000, v182
	s_nop 1
	v_addc_co_u32_e32 v183, vcc, 0, v183, vcc
	global_store_dwordx2 v[182:183], v[166:167], off
	s_waitcnt vmcnt(12)
	v_mov_b32_e32 v168, v0
	v_mov_b32_e32 v169, v0
	v_pk_mul_f32 v[120:121], v[120:121], s[20:21] op_sel_hi:[1,0]
	v_pk_mul_f32 v[116:117], v[116:117], s[20:21] op_sel_hi:[1,0]
	v_cvt_pk_fp8_f32 v169, v120, v121
	v_cvt_pk_fp8_f32 v168, v116, v117
	v_pk_mul_f32 v[118:119], v[118:119], s[20:21] op_sel_hi:[1,0]
	v_pk_mul_f32 v[122:123], v[122:123], s[20:21] op_sel_hi:[1,0]
	v_cvt_pk_fp8_f32 v168, v118, v119 op_sel:[0,0,1]
	v_cvt_pk_fp8_f32 v169, v122, v123 op_sel:[0,0,1]
	v_add_co_u32_e32 v182, vcc, 0x80000, v182
	s_nop 1
	v_addc_co_u32_e32 v183, vcc, 0, v183, vcc
	global_store_dwordx2 v[182:183], v[168:169], off
	s_waitcnt vmcnt(11)
	v_mov_b32_e32 v170, v0
	v_mov_b32_e32 v171, v0
	v_pk_mul_f32 v[128:129], v[128:129], s[20:21] op_sel_hi:[1,0]
	v_pk_mul_f32 v[124:125], v[124:125], s[20:21] op_sel_hi:[1,0]
	v_cvt_pk_fp8_f32 v171, v128, v129
	v_cvt_pk_fp8_f32 v170, v124, v125
	v_pk_mul_f32 v[126:127], v[126:127], s[20:21] op_sel_hi:[1,0]
	v_pk_mul_f32 v[130:131], v[130:131], s[20:21] op_sel_hi:[1,0]
	v_cvt_pk_fp8_f32 v170, v126, v127 op_sel:[0,0,1]
	v_cvt_pk_fp8_f32 v171, v130, v131 op_sel:[0,0,1]
	v_add_co_u32_e32 v182, vcc, 0x80000, v182
	s_nop 1
	v_addc_co_u32_e32 v183, vcc, 0, v183, vcc
	global_store_dwordx2 v[182:183], v[170:171], off
	s_waitcnt vmcnt(10)
	v_mov_b32_e32 v172, v0
	v_mov_b32_e32 v173, v0
	v_pk_mul_f32 v[136:137], v[136:137], s[20:21] op_sel_hi:[1,0]
	v_pk_mul_f32 v[132:133], v[132:133], s[20:21] op_sel_hi:[1,0]
	v_cvt_pk_fp8_f32 v173, v136, v137
	v_cvt_pk_fp8_f32 v172, v132, v133
	v_pk_mul_f32 v[134:135], v[134:135], s[20:21] op_sel_hi:[1,0]
	v_pk_mul_f32 v[138:139], v[138:139], s[20:21] op_sel_hi:[1,0]
	v_cvt_pk_fp8_f32 v172, v134, v135 op_sel:[0,0,1]
	v_cvt_pk_fp8_f32 v173, v138, v139 op_sel:[0,0,1]
	v_add_co_u32_e32 v182, vcc, 0x80000, v182
	s_nop 1
	v_addc_co_u32_e32 v183, vcc, 0, v183, vcc
	global_store_dwordx2 v[182:183], v[172:173], off
	s_waitcnt vmcnt(9)
	v_mov_b32_e32 v174, v0
	v_mov_b32_e32 v175, v0
	v_pk_mul_f32 v[144:145], v[144:145], s[20:21] op_sel_hi:[1,0]
	v_pk_mul_f32 v[140:141], v[140:141], s[20:21] op_sel_hi:[1,0]
	v_cvt_pk_fp8_f32 v175, v144, v145
	v_cvt_pk_fp8_f32 v174, v140, v141
	v_pk_mul_f32 v[142:143], v[142:143], s[20:21] op_sel_hi:[1,0]
	v_pk_mul_f32 v[146:147], v[146:147], s[20:21] op_sel_hi:[1,0]
	v_cvt_pk_fp8_f32 v174, v142, v143 op_sel:[0,0,1]
	v_cvt_pk_fp8_f32 v175, v146, v147 op_sel:[0,0,1]
	v_add_co_u32_e32 v182, vcc, 0x80000, v182
	s_nop 1
	v_addc_co_u32_e32 v183, vcc, 0, v183, vcc
	global_store_dwordx2 v[182:183], v[174:175], off
	s_waitcnt vmcnt(8)
	v_mov_b32_e32 v176, v0
	v_mov_b32_e32 v177, v0
	v_pk_mul_f32 v[152:153], v[152:153], s[20:21] op_sel_hi:[1,0]
	v_pk_mul_f32 v[148:149], v[148:149], s[20:21] op_sel_hi:[1,0]
	v_cvt_pk_fp8_f32 v177, v152, v153
	v_cvt_pk_fp8_f32 v176, v148, v149
	v_pk_mul_f32 v[150:151], v[150:151], s[20:21] op_sel_hi:[1,0]
	v_pk_mul_f32 v[154:155], v[154:155], s[20:21] op_sel_hi:[1,0]
	v_cvt_pk_fp8_f32 v176, v150, v151 op_sel:[0,0,1]
	v_cvt_pk_fp8_f32 v177, v154, v155 op_sel:[0,0,1]
	v_add_co_u32_e32 v182, vcc, 0x80000, v182
	s_nop 1
	v_addc_co_u32_e32 v183, vcc, 0, v183, vcc
	global_store_dwordx2 v[182:183], v[176:177], off
	s_waitcnt vmcnt(7)
	v_mov_b32_e32 v178, v0
	v_mov_b32_e32 v179, v0
	v_pk_mul_f32 v[160:161], v[160:161], s[20:21] op_sel_hi:[1,0]
	v_pk_mul_f32 v[156:157], v[156:157], s[20:21] op_sel_hi:[1,0]
	v_cvt_pk_fp8_f32 v179, v160, v161
	v_cvt_pk_fp8_f32 v178, v156, v157
	v_pk_mul_f32 v[158:159], v[158:159], s[20:21] op_sel_hi:[1,0]
	v_pk_mul_f32 v[162:163], v[162:163], s[20:21] op_sel_hi:[1,0]
	v_cvt_pk_fp8_f32 v178, v158, v159 op_sel:[0,0,1]
	v_cvt_pk_fp8_f32 v179, v162, v163 op_sel:[0,0,1]
	v_add_co_u32_e32 v182, vcc, 0x80000, v182
	s_nop 1
	v_addc_co_u32_e32 v183, vcc, 0, v183, vcc
	global_store_dwordx2 v[182:183], v[178:179], off
	v_readlane_b32 s20, v254, 44
	v_readlane_b32 s21, v254, 45
	s_lshl_b64 s[20:21], s[20:21], 3
	s_add_u32 s2, s2, s20
	s_addc_u32 s3, s3, s21
	s_cmp_lt_i32 s2, 0x10000
	s_cbranch_scc0 .LBB0_1197
	s_branch .LBB0_1195

; __device__ __forceinline__ u32x4 pk8(const f32x4 a, const f32x4 b) { u32x4 w; w.x = cvt_pk_bf16(a[0], a[1]); w.y = cvt_pk_bf16(a[2], a[3]); w.z = cvt_pk_bf16(b[0], b[1]); w.w = cvt_pk_bf16(b[2], b[3]); return w; }
; __device__ __forceinline__ void cvt_chunk(const float* src, bf16* dst, size_t chunk, int lane) {
;     const f32x4* s = (const f32x4*)(src + chunk * 512) + lane * 2; const f32x4 a = s[0], b = s[1];
;     *(v4u*)(dst + chunk * 512 + lane * 8) = pk8(a, b);
; }
; __device__ __forceinline__ void prep_phase(Frame& F, const Args& a, int layer, int blk, int nblk_, int part) {
;     ...
;         for (int it = gw; it < ntot; it += NGW) {
;             int r = it;
;             if (r < n2) { cvt8_chunk(ut, (unsigned char*)(db + DB_U), r, lane, 256.f); continue; } r -= n2;
;             if (r < n2) { cvt8_chunk(vt, (unsigned char*)(db + DB_V), r, lane, 64.f); continue; } r -= n2;
;             if (r < n4) { cvt_chunk(pin, (bf16*)(db + DB_PB), r, lane); continue; } r -= n4;
.LBB0_1300:
	s_andn2_b64 vcc, exec, s[22:23]
	s_cbranch_vccnz .LBB0_1302
	v_readlane_b32 s22, v254, 44
	s_cmp_lg_u32 s22, 0x400
	s_cbranch_scc1 .Lcv_p_orig
	s_add_i32 s22, s5, 0x8000
	s_and_b32 s22, s22, 0x1c00
	s_cmp_lg_u32 s22, 0
	s_cbranch_scc1 .LBB0_1302
	v_readlane_b32 s22, v254, 30
	s_add_i32 s22, s22, s36
	s_add_i32 s30, s22, 0xfe000000
	v_lshl_add_u64 v[180:181], s[30:31], 2, v[10:11]
	global_load_dwordx4 v[100:103], v[180:181], off
	global_load_dwordx4 v[104:107], v[180:181], off offset:16
	v_add_co_u32_e32 v180, vcc, 0x200000, v180
	s_nop 1
	v_addc_co_u32_e32 v181, vcc, 0, v181, vcc
	global_load_dwordx4 v[108:111], v[180:181], off
	global_load_dwordx4 v[112:115], v[180:181], off offset:16
	v_add_co_u32_e32 v180, vcc, 0x200000, v180
	s_nop 1
	v_addc_co_u32_e32 v181, vcc, 0, v181, vcc
	global_load_dwordx4 v[116:119], v[180:181], off
	global_load_dwordx4 v[120:123], v[180:181], off offset:16
	v_add_co_u32_e32 v180, vcc, 0x200000, v180
	s_nop 1
	v_addc_co_u32_e32 v181, vcc, 0, v181, vcc
	global_load_dwordx4 v[124:127], v[180:181], off
	global_load_dwordx4 v[128:131], v[180:181], off offset:16
	v_add_co_u32_e32 v180, vcc, 0x200000, v180
	s_nop 1
	v_addc_co_u32_e32 v181, vcc, 0, v181, vcc
	global_load_dwordx4 v[132:135], v[180:181], off
	global_load_dwordx4 v[136:139], v[180:181], off offset:16
	v_add_co_u32_e32 v180, vcc, 0x200000, v180
	s_nop 1
	v_addc_co_u32_e32 v181, vcc, 0, v181, vcc
	global_load_dwordx4 v[140:143], v[180:181], off
	global_load_dwordx4 v[144:147], v[180:181], off offset:16
	v_add_co_u32_e32 v180, vcc, 0x200000, v180
	s_nop 1
	v_addc_co_u32_e32 v181, vcc, 0, v181, vcc
	global_load_dwordx4 v[148:151], v[180:181], off
	global_load_dwordx4 v[152:155], v[180:181], off offset:16
	v_add_co_u32_e32 v180, vcc, 0x200000, v180
	s_nop 1
	v_addc_co_u32_e32 v181, vcc, 0, v181, vcc
	global_load_dwordx4 v[156:159], v[180:181], off
	global_load_dwordx4 v[160:163], v[180:181], off offset:16
	v_lshl_add_u64 v[182:183], s[30:31], 1, v[12:13]
	s_waitcnt vmcnt(14)
	v_cvt_pk_bf16_f32 v100, v100, v101
	v_cvt_pk_bf16_f32 v101, v102, v103
	v_cvt_pk_bf16_f32 v102, v104, v105
	v_cvt_pk_bf16_f32 v103, v106, v107
	global_store_dwordx4 v[182:183], v[100:103], off
	s_waitcnt vmcnt(13)
	v_cvt_pk_bf16_f32 v108, v108, v109
	v_cvt_pk_bf16_f32 v109, v110, v111
	v_cvt_pk_bf16_f32 v110, v112, v113
	v_cvt_pk_bf16_f32 v111, v114, v115
	v_add_co_u32_e32 v182, vcc, 0x100000, v182
	s_nop 1
	v_addc_co_u32_e32 v183, vcc, 0, v183, vcc
	global_store_dwordx4 v[182:183], v[108:111], off
	s_waitcnt vmcnt(12)
	v_cvt_pk_bf16_f32 v116, v116, v117
	v_cvt_pk_bf16_f32 v117, v118, v119
	v_cvt_pk_bf16_f32 v118, v120, v121
	v_cvt_pk_bf16_f32 v119, v122, v123
	v_add_co_u32_e32 v182, vcc, 0x100000, v182
	s_nop 1
	v_addc_co_u32_e32 v183, vcc, 0, v183, vcc
	global_store_dwordx4 v[182:183], v[116:119], off
	s_waitcnt vmcnt(11)
	v_cvt_pk_bf16_f32 v124, v124, v125
	v_cvt_pk_bf16_f32 v125, v126, v127
	v_cvt_pk_bf16_f32 v126, v128, v129
	v_cvt_pk_bf16_f32 v127, v130, v131
	v_add_co_u32_e32 v182, vcc, 0x100000, v182
	s_nop 1
	v_addc_co_u32_e32 v183, vcc, 0, v183, vcc
	global_store_dwordx4 v[182:183], v[124:127], off
	s_waitcnt vmcnt(10)
	v_cvt_pk_bf16_f32 v132, v132, v133
	v_cvt_pk_bf16_f32 v133, v134, v135
	v_cvt_pk_bf16_f32 v134, v136, v137
	v_cvt_pk_bf16_f32 v135, v138, v139
	v_add_co_u32_e32 v182, vcc, 0x100000, v182
	s_nop 1
	v_addc_co_u32_e32 v183, vcc, 0, v183, vcc
	global_store_dwordx4 v[182:183], v[132:135], off
	s_waitcnt vmcnt(9)
	v_cvt_pk_bf16_f32 v140, v140, v141
	v_cvt_pk_bf16_f32 v141, v142, v143
	v_cvt_pk_bf16_f32 v142, v144, v145
	v_cvt_pk_bf16_f32 v143, v146, v147
	v_add_co_u32_e32 v182, vcc, 0x100000, v182
	s_nop 1
	v_addc_co_u32_e32 v183, vcc, 0, v183, vcc
	global_store_dwordx4 v[182:183], v[140:143], off
	s_waitcnt vmcnt(8)
	v_cvt_pk_bf16_f32 v148, v148, v149
	v_cvt_pk_bf16_f32 v149, v150, v151
	v_cvt_pk_bf16_f32 v150, v152, v153
	v_cvt_pk_bf16_f32 v151, v154, v155
	v_add_co_u32_e32 v182, vcc, 0x100000, v182
	s_nop 1
	v_addc_co_u32_e32 v183, vcc, 0, v183, vcc
	global_store_dwordx4 v[182:183], v[148:151], off
	s_waitcnt vmcnt(7)
	v_cvt_pk_bf16_f32 v156, v156, v157
	v_cvt_pk_bf16_f32 v157, v158, v159
	v_cvt_pk_bf16_f32 v158, v160, v161
	v_cvt_pk_bf16_f32 v159, v162, v163
	v_add_co_u32_e32 v182, vcc, 0x100000, v182
	s_nop 1
	v_addc_co_u32_e32 v183, vcc, 0, v183, vcc
	global_store_dwordx4 v[182:183], v[156:159], off
	s_branch .LBB0_1302

; __device__ __forceinline__ void cvt8_chunk(const float* src, unsigned char* dst, size_t chunk, int lane, float sc) {
;     const f32x4* s = (const f32x4*)(src + chunk * 512) + lane * 2; const f32x4 a = s[0] * sc, b = s[1] * sc;
;     int w0 = 0, w1 = 0;
;     w0 = __builtin_amdgcn_cvt_pk_fp8_f32(a.x, a.y, w0, false); w0 = __builtin_amdgcn_cvt_pk_fp8_f32(a.z, a.w, w0, true);
;     w1 = __builtin_amdgcn_cvt_pk_fp8_f32(b.x, b.y, w1, false); w1 = __builtin_amdgcn_cvt_pk_fp8_f32(b.z, b.w, w1, true);
;     *(v2u*)(dst + chunk * 512 + lane * 8) = (v2u){(unsigned)w0, (unsigned)w1};
; }
; __device__ __forceinline__ void prep_phase(Frame& F, const Args& a, int layer, int blk, int nblk_, int part) {
;     ...
;         for (int it = gw; it < ntot; it += NGW) {
;             int r = it;
;             if (r < n2) { cvt8_chunk(ut, (unsigned char*)(db + DB_U), r, lane, 256.f); continue; } r -= n2;
;             if (r < n2) { cvt8_chunk(vt, (unsigned char*)(db + DB_V), r, lane, 64.f); continue; } r -= n2;
.LBB0_1303:
	s_andn2_b64 vcc, exec, s[22:23]
	s_cbranch_vccnz .LBB0_1305
	v_readlane_b32 s22, v254, 44
	s_cmp_lg_u32 s22, 0x400
	s_cbranch_scc1 .Lcv_v_orig
	s_add_i32 s22, s5, 0x8000
	s_and_b32 s22, s22, 0x1c00
	s_cmp_lg_u32 s22, 0
	s_cbranch_scc1 .LBB0_1305
	v_readlane_b32 s22, v254, 30
	s_add_i32 s22, s22, s36
	s_add_i32 s30, s22, 0xff000000
	v_lshl_add_u64 v[180:181], s[30:31], 2, v[14:15]
	s_mov_b32 s22, 0x42800000
	global_load_dwordx4 v[104:107], v[180:181], off offset:16
	global_load_dwordx4 v[100:103], v[180:181], off
	v_add_co_u32_e32 v180, vcc, 0x200000, v180
	s_nop 1
	v_addc_co_u32_e32 v181, vcc, 0, v181, vcc
	global_load_dwordx4 v[112:115], v[180:181], off offset:16
	global_load_dwordx4 v[108:111], v[180:181], off
	v_add_co_u32_e32 v180, vcc, 0x200000, v180
	s_nop 1
	v_addc_co_u32_e32 v181, vcc, 0, v181, vcc
	global_load_dwordx4 v[120:123], v[180:181], off offset:16
	global_load_dwordx4 v[116:119], v[180:181], off
	v_add_co_u32_e32 v180, vcc, 0x200000, v180
	s_nop 1
	v_addc_co_u32_e32 v181, vcc, 0, v181, vcc
	global_load_dwordx4 v[128:131], v[180:181], off offset:16
	global_load_dwordx4 v[124:127], v[180:181], off
	v_add_co_u32_e32 v180, vcc, 0x200000, v180
	s_nop 1
	v_addc_co_u32_e32 v181, vcc, 0, v181, vcc
	global_load_dwordx4 v[136:139], v[180:181], off offset:16
	global_load_dwordx4 v[132:135], v[180:181], off
	v_add_co_u32_e32 v180, vcc, 0x200000, v180
	s_nop 1
	v_addc_co_u32_e32 v181, vcc, 0, v181, vcc
	global_load_dwordx4 v[144:147], v[180:181], off offset:16
	global_load_dwordx4 v[140:143], v[180:181], off
	v_add_co_u32_e32 v180, vcc, 0x200000, v180
	s_nop 1
	v_addc_co_u32_e32 v181, vcc, 0, v181, vcc
	global_load_dwordx4 v[152:155], v[180:181], off offset:16
	global_load_dwordx4 v[148:151], v[180:181], off
	v_add_co_u32_e32 v180, vcc, 0x200000, v180
	s_nop 1
	v_addc_co_u32_e32 v181, vcc, 0, v181, vcc
	global_load_dwordx4 v[160:163], v[180:181], off offset:16
	global_load_dwordx4 v[156:159], v[180:181], off
	v_lshl_add_u64 v[182:183], v[16:17], 0, s[30:31]
	s_waitcnt vmcnt(14)
	v_mov_b32_e32 v164, v0
	v_mov_b32_e32 v165, v0
	v_pk_mul_f32 v[104:105], v[104:105], s[22:23] op_sel_hi:[1,0]
	v_pk_mul_f32 v[100:101], v[100:101], s[22:23] op_sel_hi:[1,0]
	v_cvt_pk_fp8_f32 v165, v104, v105
	v_cvt_pk_fp8_f32 v164, v100, v101
	v_pk_mul_f32 v[102:103], v[102:103], s[22:23] op_sel_hi:[1,0]
	v_pk_mul_f32 v[106:107], v[106:107], s[22:23] op_sel_hi:[1,0]
	v_cvt_pk_fp8_f32 v164, v102, v103 op_sel:[0,0,1]
	v_cvt_pk_fp8_f32 v165, v106, v107 op_sel:[0,0,1]
	global_store_dwordx2 v[182:183], v[164:165], off
	s_waitcnt vmcnt(13)
	v_mov_b32_e32 v166, v0
	v_mov_b32_e32 v167, v0
	v_pk_mul_f32 v[112:113], v[112:113], s[22:23] op_sel_hi:[1,0]
	v_pk_mul_f32 v[108:109], v[108:109], s[22:23] op_sel_hi:[1,0]
	v_cvt_pk_fp8_f32 v167, v112, v113
	v_cvt_pk_fp8_f32 v166, v108, v109
	v_pk_mul_f32 v[110:111], v[110:111], s[22:23] op_sel_hi:[1,0]
	v_pk_mul_f32 v[114:115], v[114:115], s[22:23] op_sel_hi:[1,0]
	v_cvt_pk_fp8_f32 v166, v110, v111 op_sel:[0,0,1]
	v_cvt_pk_fp8_f32 v167, v114, v115 op_sel:[0,0,1]
	v_add_co_u32_e32 v182, vcc, 0x80000, v182
	s_nop 1
	v_addc_co_u32_e32 v183, vcc, 0, v183, vcc
	global_store_dwordx2 v[182:183], v[166:167], off
	s_waitcnt vmcnt(12)
	v_mov_b32_e32 v168, v0
	v_mov_b32_e32 v169, v0
	v_pk_mul_f32 v[120:121], v[120:121], s[22:23] op_sel_hi:[1,0]
	v_pk_mul_f32 v[116:117], v[116:117], s[22:23] op_sel_hi:[1,0]
	v_cvt_pk_fp8_f32 v169, v120, v121
	v_cvt_pk_fp8_f32 v168, v116, v117
	v_pk_mul_f32 v[118:119], v[118:119], s[22:23] op_sel_hi:[1,0]
	v_pk_mul_f32 v[122:123], v[122:123], s[22:23] op_sel_hi:[1,0]
	v_cvt_pk_fp8_f32 v168, v118, v119 op_sel:[0,0,1]
	v_cvt_pk_fp8_f32 v169, v122, v123 op_sel:[0,0,1]
	v_add_co_u32_e32 v182, vcc, 0x80000, v182
	s_nop 1
	v_addc_co_u32_e32 v183, vcc, 0, v183, vcc
	global_store_dwordx2 v[182:183], v[168:169], off
	s_waitcnt vmcnt(11)
	v_mov_b32_e32 v170, v0
	v_mov_b32_e32 v171, v0
	v_pk_mul_f32 v[128:129], v[128:129], s[22:23] op_sel_hi:[1,0]
	v_pk_mul_f32 v[124:125], v[124:125], s[22:23] op_sel_hi:[1,0]
	v_cvt_pk_fp8_f32 v171, v128, v129
	v_cvt_pk_fp8_f32 v170, v124, v125
	v_pk_mul_f32 v[126:127], v[126:127], s[22:23] op_sel_hi:[1,0]
	v_pk_mul_f32 v[130:131], v[130:131], s[22:23] op_sel_hi:[1,0]
	v_cvt_pk_fp8_f32 v170, v126, v127 op_sel:[0,0,1]
	v_cvt_pk_fp8_f32 v171, v130, v131 op_sel:[0,0,1]
	v_add_co_u32_e32 v182, vcc, 0x80000, v182
	s_nop 1
	v_addc_co_u32_e32 v183, vcc, 0, v183, vcc
	global_store_dwordx2 v[182:183], v[170:171], off
	s_waitcnt vmcnt(10)
	v_mov_b32_e32 v172, v0
	v_mov_b32_e32 v173, v0
	v_pk_mul_f32 v[136:137], v[136:137], s[22:23] op_sel_hi:[1,0]
	v_pk_mul_f32 v[132:133], v[132:133], s[22:23] op_sel_hi:[1,0]
	v_cvt_pk_fp8_f32 v173, v136, v137
	v_cvt_pk_fp8_f32 v172, v132, v133
	v_pk_mul_f32 v[134:135], v[134:135], s[22:23] op_sel_hi:[1,0]
	v_pk_mul_f32 v[138:139], v[138:139], s[22:23] op_sel_hi:[1,0]
	v_cvt_pk_fp8_f32 v172, v134, v135 op_sel:[0,0,1]
	v_cvt_pk_fp8_f32 v173, v138, v139 op_sel:[0,0,1]
	v_add_co_u32_e32 v182, vcc, 0x80000, v182
	s_nop 1
	v_addc_co_u32_e32 v183, vcc, 0, v183, vcc
	global_store_dwordx2 v[182:183], v[172:173], off
	s_waitcnt vmcnt(9)
	v_mov_b32_e32 v174, v0
	v_mov_b32_e32 v175, v0
	v_pk_mul_f32 v[144:145], v[144:145], s[22:23] op_sel_hi:[1,0]
	v_pk_mul_f32 v[140:141], v[140:141], s[22:23] op_sel_hi:[1,0]
	v_cvt_pk_fp8_f32 v175, v144, v145
	v_cvt_pk_fp8_f32 v174, v140, v141
	v_pk_mul_f32 v[142:143], v[142:143], s[22:23] op_sel_hi:[1,0]
	v_pk_mul_f32 v[146:147], v[146:147], s[22:23] op_sel_hi:[1,0]
	v_cvt_pk_fp8_f32 v174, v142, v143 op_sel:[0,0,1]
	v_cvt_pk_fp8_f32 v175, v146, v147 op_sel:[0,0,1]
	v_add_co_u32_e32 v182, vcc, 0x80000, v182
	s_nop 1
	v_addc_co_u32_e32 v183, vcc, 0, v183, vcc
	global_store_dwordx2 v[182:183], v[174:175], off
	s_waitcnt vmcnt(8)
	v_mov_b32_e32 v176, v0
	v_mov_b32_e32 v177, v0
	v_pk_mul_f32 v[152:153], v[152:153], s[22:23] op_sel_hi:[1,0]
	v_pk_mul_f32 v[148:149], v[148:149], s[22:23] op_sel_hi:[1,0]
	v_cvt_pk_fp8_f32 v177, v152, v153
	v_cvt_pk_fp8_f32 v176, v148, v149
	v_pk_mul_f32 v[150:151], v[150:151], s[22:23] op_sel_hi:[1,0]
	v_pk_mul_f32 v[154:155], v[154:155], s[22:23] op_sel_hi:[1,0]
	v_cvt_pk_fp8_f32 v176, v150, v151 op_sel:[0,0,1]
	v_cvt_pk_fp8_f32 v177, v154, v155 op_sel:[0,0,1]
	v_add_co_u32_e32 v182, vcc, 0x80000, v182
	s_nop 1
	v_addc_co_u32_e32 v183, vcc, 0, v183, vcc
	global_store_dwordx2 v[182:183], v[176:177], off
	s_waitcnt vmcnt(7)
	v_mov_b32_e32 v178, v0
	v_mov_b32_e32 v179, v0
	v_pk_mul_f32 v[160:161], v[160:161], s[22:23] op_sel_hi:[1,0]
	v_pk_mul_f32 v[156:157], v[156:157], s[22:23] op_sel_hi:[1,0]
	v_cvt_pk_fp8_f32 v179, v160, v161
	v_cvt_pk_fp8_f32 v178, v156, v157
	v_pk_mul_f32 v[158:159], v[158:159], s[22:23] op_sel_hi:[1,0]
	v_pk_mul_f32 v[162:163], v[162:163], s[22:23] op_sel_hi:[1,0]
	v_cvt_pk_fp8_f32 v178, v158, v159 op_sel:[0,0,1]
	v_cvt_pk_fp8_f32 v179, v162, v163 op_sel:[0,0,1]
	v_add_co_u32_e32 v182, vcc, 0x80000, v182
	s_nop 1
	v_addc_co_u32_e32 v183, vcc, 0, v183, vcc
	global_store_dwordx2 v[182:183], v[178:179], off
	s_branch .LBB0_1305

; __device__ __forceinline__ void cvt8_chunk(const float* src, unsigned char* dst, size_t chunk, int lane, float sc) {
;     const f32x4* s = (const f32x4*)(src + chunk * 512) + lane * 2; const f32x4 a = s[0] * sc, b = s[1] * sc;
;     int w0 = 0, w1 = 0;
;     w0 = __builtin_amdgcn_cvt_pk_fp8_f32(a.x, a.y, w0, false); w0 = __builtin_amdgcn_cvt_pk_fp8_f32(a.z, a.w, w0, true);
;     w1 = __builtin_amdgcn_cvt_pk_fp8_f32(b.x, b.y, w1, false); w1 = __builtin_amdgcn_cvt_pk_fp8_f32(b.z, b.w, w1, true);
;     *(v2u*)(dst + chunk * 512 + lane * 8) = (v2u){(unsigned)w0, (unsigned)w1};
; }
; __device__ __forceinline__ void prep_phase(Frame& F, const Args& a, int layer, int blk, int nblk_, int part) {
;     ...
;         for (int it = gw; it < ntot; it += NGW) {
;             int r = it;
;             if (r < n2) { cvt8_chunk(ut, (unsigned char*)(db + DB_U), r, lane, 256.f); continue; } r -= n2;
.LBB0_1306:
	s_andn2_b64 vcc, exec, s[22:23]
	s_cbranch_vccnz .LBB0_1291
	v_readlane_b32 s22, v254, 44
	s_cmp_lg_u32 s22, 0x400
	s_cbranch_scc1 .Lcv_u_orig
	s_add_i32 s22, s5, 0x8000
	s_and_b32 s22, s22, 0x1c00
	s_cmp_lg_u32 s22, 0
	s_cbranch_scc1 .LBB0_1291
	v_lshl_add_u64 v[180:181], s[20:21], 0, v[4:5]
	global_load_dwordx4 v[104:107], v[180:181], off offset:16
	global_load_dwordx4 v[100:103], v[180:181], off
	v_add_co_u32_e32 v180, vcc, 0x200000, v180
	s_nop 1
	v_addc_co_u32_e32 v181, vcc, 0, v181, vcc
	global_load_dwordx4 v[112:115], v[180:181], off offset:16
	global_load_dwordx4 v[108:111], v[180:181], off
	v_add_co_u32_e32 v180, vcc, 0x200000, v180
	s_nop 1
	v_addc_co_u32_e32 v181, vcc, 0, v181, vcc
	global_load_dwordx4 v[120:123], v[180:181], off offset:16
	global_load_dwordx4 v[116:119], v[180:181], off
	v_add_co_u32_e32 v180, vcc, 0x200000, v180
	s_nop 1
	v_addc_co_u32_e32 v181, vcc, 0, v181, vcc
	global_load_dwordx4 v[128:131], v[180:181], off offset:16
	global_load_dwordx4 v[124:127], v[180:181], off
	v_add_co_u32_e32 v180, vcc, 0x200000, v180
	s_nop 1
	v_addc_co_u32_e32 v181, vcc, 0, v181, vcc
	global_load_dwordx4 v[136:139], v[180:181], off offset:16
	global_load_dwordx4 v[132:135], v[180:181], off
	v_add_co_u32_e32 v180, vcc, 0x200000, v180
	s_nop 1
	v_addc_co_u32_e32 v181, vcc, 0, v181, vcc
	global_load_dwordx4 v[144:147], v[180:181], off offset:16
	global_load_dwordx4 v[140:143], v[180:181], off
	v_add_co_u32_e32 v180, vcc, 0x200000, v180
	s_nop 1
	v_addc_co_u32_e32 v181, vcc, 0, v181, vcc
	global_load_dwordx4 v[152:155], v[180:181], off offset:16
	global_load_dwordx4 v[148:151], v[180:181], off
	v_add_co_u32_e32 v180, vcc, 0x200000, v180
	s_nop 1
	v_addc_co_u32_e32 v181, vcc, 0, v181, vcc
	global_load_dwordx4 v[160:163], v[180:181], off offset:16
	global_load_dwordx4 v[156:159], v[180:181], off
	v_mov_b64_e32 v[182:183], v[2:3]
	s_waitcnt vmcnt(14)
	v_mov_b32_e32 v164, v0
	v_mov_b32_e32 v165, v0
	v_pk_mul_f32 v[104:105], v[104:105], s[8:9] op_sel_hi:[1,0]
	v_pk_mul_f32 v[100:101], v[100:101], s[8:9] op_sel_hi:[1,0]
	v_cvt_pk_fp8_f32 v165, v104, v105
	v_cvt_pk_fp8_f32 v164, v100, v101
	v_pk_mul_f32 v[102:103], v[102:103], s[8:9] op_sel_hi:[1,0]
	v_pk_mul_f32 v[106:107], v[106:107], s[8:9] op_sel_hi:[1,0]
	v_cvt_pk_fp8_f32 v164, v102, v103 op_sel:[0,0,1]
	v_cvt_pk_fp8_f32 v165, v106, v107 op_sel:[0,0,1]
	global_store_dwordx2 v[182:183], v[164:165], off
	s_waitcnt vmcnt(13)
	v_mov_b32_e32 v166, v0
	v_mov_b32_e32 v167, v0
	v_pk_mul_f32 v[112:113], v[112:113], s[8:9] op_sel_hi:[1,0]
	v_pk_mul_f32 v[108:109], v[108:109], s[8:9] op_sel_hi:[1,0]
	v_cvt_pk_fp8_f32 v167, v112, v113
	v_cvt_pk_fp8_f32 v166, v108, v109
	v_pk_mul_f32 v[110:111], v[110:111], s[8:9] op_sel_hi:[1,0]
	v_pk_mul_f32 v[114:115], v[114:115], s[8:9] op_sel_hi:[1,0]
	v_cvt_pk_fp8_f32 v166, v110, v111 op_sel:[0,0,1]
	v_cvt_pk_fp8_f32 v167, v114, v115 op_sel:[0,0,1]
	v_add_co_u32_e32 v182, vcc, 0x80000, v182
	s_nop 1
	v_addc_co_u32_e32 v183, vcc, 0, v183, vcc
	global_store_dwordx2 v[182:183], v[166:167], off
	s_waitcnt vmcnt(12)
	v_mov_b32_e32 v168, v0
	v_mov_b32_e32 v169, v0
	v_pk_mul_f32 v[120:121], v[120:121], s[8:9] op_sel_hi:[1,0]
	v_pk_mul_f32 v[116:117], v[116:117], s[8:9] op_sel_hi:[1,0]
	v_cvt_pk_fp8_f32 v169, v120, v121
	v_cvt_pk_fp8_f32 v168, v116, v117
	v_pk_mul_f32 v[118:119], v[118:119], s[8:9] op_sel_hi:[1,0]
	v_pk_mul_f32 v[122:123], v[122:123], s[8:9] op_sel_hi:[1,0]
	v_cvt_pk_fp8_f32 v168, v118, v119 op_sel:[0,0,1]
	v_cvt_pk_fp8_f32 v169, v122, v123 op_sel:[0,0,1]
	v_add_co_u32_e32 v182, vcc, 0x80000, v182
	s_nop 1
	v_addc_co_u32_e32 v183, vcc, 0, v183, vcc
	global_store_dwordx2 v[182:183], v[168:169], off
	s_waitcnt vmcnt(11)
	v_mov_b32_e32 v170, v0
	v_mov_b32_e32 v171, v0
	v_pk_mul_f32 v[128:129], v[128:129], s[8:9] op_sel_hi:[1,0]
	v_pk_mul_f32 v[124:125], v[124:125], s[8:9] op_sel_hi:[1,0]
	v_cvt_pk_fp8_f32 v171, v128, v129
	v_cvt_pk_fp8_f32 v170, v124, v125
	v_pk_mul_f32 v[126:127], v[126:127], s[8:9] op_sel_hi:[1,0]
	v_pk_mul_f32 v[130:131], v[130:131], s[8:9] op_sel_hi:[1,0]
	v_cvt_pk_fp8_f32 v170, v126, v127 op_sel:[0,0,1]
	v_cvt_pk_fp8_f32 v171, v130, v131 op_sel:[0,0,1]
	v_add_co_u32_e32 v182, vcc, 0x80000, v182
	s_nop 1
	v_addc_co_u32_e32 v183, vcc, 0, v183, vcc
	global_store_dwordx2 v[182:183], v[170:171], off
	s_waitcnt vmcnt(10)
	v_mov_b32_e32 v172, v0
	v_mov_b32_e32 v173, v0
	v_pk_mul_f32 v[136:137], v[136:137], s[8:9] op_sel_hi:[1,0]
	v_pk_mul_f32 v[132:133], v[132:133], s[8:9] op_sel_hi:[1,0]
	v_cvt_pk_fp8_f32 v173, v136, v137
	v_cvt_pk_fp8_f32 v172, v132, v133
	v_pk_mul_f32 v[134:135], v[134:135], s[8:9] op_sel_hi:[1,0]
	v_pk_mul_f32 v[138:139], v[138:139], s[8:9] op_sel_hi:[1,0]
	v_cvt_pk_fp8_f32 v172, v134, v135 op_sel:[0,0,1]
	v_cvt_pk_fp8_f32 v173, v138, v139 op_sel:[0,0,1]
	v_add_co_u32_e32 v182, vcc, 0x80000, v182
	s_nop 1
	v_addc_co_u32_e32 v183, vcc, 0, v183, vcc
	global_store_dwordx2 v[182:183], v[172:173], off
	s_waitcnt vmcnt(9)
	v_mov_b32_e32 v174, v0
	v_mov_b32_e32 v175, v0
	v_pk_mul_f32 v[144:145], v[144:145], s[8:9] op_sel_hi:[1,0]
	v_pk_mul_f32 v[140:141], v[140:141], s[8:9] op_sel_hi:[1,0]
	v_cvt_pk_fp8_f32 v175, v144, v145
	v_cvt_pk_fp8_f32 v174, v140, v141
	v_pk_mul_f32 v[142:143], v[142:143], s[8:9] op_sel_hi:[1,0]
	v_pk_mul_f32 v[146:147], v[146:147], s[8:9] op_sel_hi:[1,0]
	v_cvt_pk_fp8_f32 v174, v142, v143 op_sel:[0,0,1]
	v_cvt_pk_fp8_f32 v175, v146, v147 op_sel:[0,0,1]
	v_add_co_u32_e32 v182, vcc, 0x80000, v182
	s_nop 1
	v_addc_co_u32_e32 v183, vcc, 0, v183, vcc
	global_store_dwordx2 v[182:183], v[174:175], off
	s_waitcnt vmcnt(8)
	v_mov_b32_e32 v176, v0
	v_mov_b32_e32 v177, v0
	v_pk_mul_f32 v[152:153], v[152:153], s[8:9] op_sel_hi:[1,0]
	v_pk_mul_f32 v[148:149], v[148:149], s[8:9] op_sel_hi:[1,0]
	v_cvt_pk_fp8_f32 v177, v152, v153
	v_cvt_pk_fp8_f32 v176, v148, v149
	v_pk_mul_f32 v[150:151], v[150:151], s[8:9] op_sel_hi:[1,0]
	v_pk_mul_f32 v[154:155], v[154:155], s[8:9] op_sel_hi:[1,0]
	v_cvt_pk_fp8_f32 v176, v150, v151 op_sel:[0,0,1]
	v_cvt_pk_fp8_f32 v177, v154, v155 op_sel:[0,0,1]
	v_add_co_u32_e32 v182, vcc, 0x80000, v182
	s_nop 1
	v_addc_co_u32_e32 v183, vcc, 0, v183, vcc
	global_store_dwordx2 v[182:183], v[176:177], off
	s_waitcnt vmcnt(7)
	v_mov_b32_e32 v178, v0
	v_mov_b32_e32 v179, v0
	v_pk_mul_f32 v[160:161], v[160:161], s[8:9] op_sel_hi:[1,0]
	v_pk_mul_f32 v[156:157], v[156:157], s[8:9] op_sel_hi:[1,0]
	v_cvt_pk_fp8_f32 v179, v160, v161
	v_cvt_pk_fp8_f32 v178, v156, v157
	v_pk_mul_f32 v[158:159], v[158:159], s[8:9] op_sel_hi:[1,0]
	v_pk_mul_f32 v[162:163], v[162:163], s[8:9] op_sel_hi:[1,0]
	v_cvt_pk_fp8_f32 v178, v158, v159 op_sel:[0,0,1]
	v_cvt_pk_fp8_f32 v179, v162, v163 op_sel:[0,0,1]
	v_add_co_u32_e32 v182, vcc, 0x80000, v182
	s_nop 1
	v_addc_co_u32_e32 v183, vcc, 0, v183, vcc
	global_store_dwordx2 v[182:183], v[178:179], off
	s_branch .LBB0_1291

; #define LAS __attribute__((address_space(3)))
; #define U_RANGE(T, P, RLO, RHI, BLO, BHI) PL_RANGE4(T, P, RLO, RHI, BLO, BHI)
; __device__ __forceinline__ void peer_unit(Frame& F, const Args& a, int layer, int unit, bool last) {
;     ...
;     for (int it = 0; it < 16; ++it) {
;         const v4u se = se_pf;
;         if (it < 15) se_pf = *(const v4u*)(SELW + (tokb + it + 1) * 256 + 4 * lane);
;         const unsigned b0 = se.x >> 12, b1 = se.z >> 12;
;         unsigned pos0 = 0u, pos1 = 0u, base = 0u, pk = 0u;
; #pragma unroll
;         for (unsigned k = 0; k < 4; ++k) {
;             const unsigned long long m0 = __builtin_amdgcn_ballot_w64(b0 == k), m1 = __builtin_amdgcn_ballot_w64(b1 == k);
;             const unsigned below = __builtin_amdgcn_mbcnt_hi((unsigned)(m0 >> 32), __builtin_amdgcn_mbcnt_lo((unsigned)m0, 0u)) + __builtin_amdgcn_mbcnt_hi((unsigned)(m1 >> 32), __builtin_amdgcn_mbcnt_lo((unsigned)m1, 0u));
;             if (b0 == k) pos0 = base + below;
;             if (b1 == k) pos1 = base + below + (b0 == k ? 1u : 0u);
;             base += (unsigned)__builtin_popcountll(m0) + (unsigned)__builtin_popcountll(m1);
;             if (k < 3) pk |= base << (8 * k);
;         }
;     ...
;         pos0 = 2 * lane; pos1 = 2 * lane + 1;
;     ...
;         *(LAS v2u*)(sSort + 2 * pos0) = (v2u){se.x, se.y}; *(LAS v2u*)(sSort + 2 * pos1) = (v2u){se.z, se.w};
;         asm volatile("" ::: "memory");
;         const v2u so0 = *(const LAS v2u*)(sSort + 4 * lane), so1 = *(const LAS v2u*)(sSort + 4 * lane + 2); const v4u so = (v4u){so0.x, so0.y, so1.x, so1.y};
;         asm volatile("" ::: "memory");
;         sIdx[it * 64 + lane] = (so0.x & 0xffffu) | (so1.x << 16);
;         (void)so;
;         { const unsigned g0 = so0.y, g1 = so1.y; sCoef[it * 128 + 2 * lane] = __uint_as_float(g0); sCoef[it * 128 + 2 * lane + 1] = __uint_as_float(g1); }
;         if (lane == it) cnts = pk;
;     }
;     ...
;     for (int ps = DBG_U0; ps < UPASS; ++ps) {
;         int lt = 0, lb, lbh; { U_RANGE(lt, ps, r0, r1, b0_, b1_); lb = b0_; lbh = b1_; (void)r0; (void)r1; }
;         unsigned seL = sIdx[lane];
;         long xlo = 0, xhi = 0; const bool dsel = ((lane >> 2) & 3) == (lane >> 4); const unsigned char* N8 = (const unsigned char*)(F.ws + WS_N8); v4u nnx = *(const v4u*)(N8 + tokb * 1024 + 16 * lane);
;         int ct, cb, crl = 0, crh = 0, cbl = 0;
.LBB0_1726:
	s_waitcnt vmcnt(0)
	v_mov_b64_e32 v[16:17], v[4:5]
	v_mov_b64_e32 v[14:15], v[2:3]
	global_load_dwordx4 v[2:5], v[6:7], off
	v_cmp_gt_u32_e32 vcc, s9, v14
	v_cmp_gt_u32_e64 s[38:39], s9, v16
	v_lshrrev_b32_e32 v13, 12, v14
	v_mbcnt_lo_u32_b32 v19, vcc_lo, 0
	v_mbcnt_lo_u32_b32 v20, s38, 0
	v_mbcnt_hi_u32_b32 v19, vcc_hi, v19
	v_mbcnt_hi_u32_b32 v20, s39, v20
	v_add_u32_e32 v21, v20, v19
	v_lshrrev_b32_e32 v18, 12, v16
	v_cndmask_b32_e32 v21, 0, v21, vcc
	v_addc_co_u32_e64 v19, s[40:41], v20, v19, vcc
	s_bcnt1_i32_b64 s5, vcc
	v_cmp_eq_u32_e32 vcc, 1, v13
	v_cndmask_b32_e64 v19, 0, v19, s[38:39]
	s_bcnt1_i32_b64 s30, s[38:39]
	v_cmp_eq_u32_e64 s[38:39], 1, v18
	v_mbcnt_lo_u32_b32 v20, vcc_lo, 0
	s_add_i32 s5, s30, s5
	v_mbcnt_hi_u32_b32 v20, vcc_hi, v20
	v_mbcnt_lo_u32_b32 v22, s38, 0
	v_mbcnt_hi_u32_b32 v22, s39, v22
	v_add_u32_e32 v20, s5, v20
	v_add_u32_e32 v23, v20, v22
	v_addc_co_u32_e64 v20, s[40:41], v20, v22, vcc
	s_bcnt1_i32_b64 s30, vcc
	v_cndmask_b32_e32 v21, v21, v23, vcc
	v_cndmask_b32_e64 v19, v19, v20, s[38:39]
	s_bcnt1_i32_b64 s38, s[38:39]
	s_add_i32 s30, s5, s30
	v_cmp_eq_u32_e32 vcc, 2, v13
	s_add_i32 s30, s30, s38
	v_cmp_eq_u32_e64 s[38:39], 2, v18
	v_mbcnt_lo_u32_b32 v20, vcc_lo, 0
	v_mbcnt_hi_u32_b32 v20, vcc_hi, v20
	v_mbcnt_lo_u32_b32 v22, s38, 0
	v_mbcnt_hi_u32_b32 v22, s39, v22
	v_add_u32_e32 v20, s30, v20
	v_add_u32_e32 v23, v20, v22
	v_addc_co_u32_e64 v20, s[40:41], v20, v22, vcc
	s_bcnt1_i32_b64 s40, vcc
	s_lshl_b32 s42, s30, 8
	v_cndmask_b32_e32 v21, v21, v23, vcc
	v_cndmask_b32_e64 v19, v19, v20, s[38:39]
	s_bcnt1_i32_b64 s38, s[38:39]
	s_add_i32 s30, s30, s40
	v_cmp_eq_u32_e32 vcc, 3, v13
	s_add_i32 s30, s30, s38
	v_cmp_eq_u32_e64 s[38:39], 3, v18
	v_mbcnt_lo_u32_b32 v13, vcc_lo, 0
	v_mbcnt_hi_u32_b32 v13, vcc_hi, v13
	v_mbcnt_lo_u32_b32 v18, s38, 0
	v_mbcnt_hi_u32_b32 v18, s39, v18
	v_add_u32_e32 v13, s30, v13
	v_add_u32_e32 v20, v13, v18
	v_cndmask_b32_e32 v20, v21, v20, vcc
	v_addc_co_u32_e32 v13, vcc, v13, v18, vcc
	v_cndmask_b32_e64 v13, v19, v13, s[38:39]
	v_lshl_add_u32 v18, v20, 3, s33
	v_lshl_add_u32 v13, v13, 3, s33
	ds_write_b64 v18, v[14:15]
	ds_write_b64 v13, v[16:17]
	ds_read_b128 v[14:17], v10
	s_lshl_b32 s30, s30, 16
	s_or_b32 s30, s42, s30
	s_or_b32 s5, s30, s5
	s_waitcnt lgkmcnt(0)
	v_and_b32_e32 v13, 0xffff, v14
	v_lshl_or_b32 v13, v16, 16, v13
	ds_write_b32 v11, v13
	v_mov_b32_e32 v16, v15
	v_mov_b32_e32 v13, s5
	v_cmp_eq_u32_e32 vcc, s3, v74
	s_add_i32 s3, s3, 1
	s_mov_b64 s[38:39], 0x400
	ds_write_b64 v12, v[16:17]
	v_cndmask_b32_e32 v9, v9, v13, vcc
	v_add_u32_e32 v12, 0x200, v12
	v_add_u32_e32 v11, 0x100, v11
	s_cmp_eq_u32 s3, 15
	v_lshl_add_u64 v[6:7], v[6:7], 0, s[38:39]
	s_cbranch_scc0 .LBB0_1726
	s_waitcnt vmcnt(0)
	v_cmp_gt_u32_e32 vcc, s9, v2
	v_cmp_gt_u32_e64 s[38:39], s9, v4
	s_add_u32 s3, s18, s76
	v_mbcnt_lo_u32_b32 v11, vcc_lo, 0
	v_mbcnt_lo_u32_b32 v12, s38, 0
	s_addc_u32 s5, s19, 0
	v_mbcnt_hi_u32_b32 v11, vcc_hi, v11
	v_mbcnt_hi_u32_b32 v12, s39, v12
	s_add_u32 s42, s3, 0x2800000
	v_lshrrev_b32_e32 v6, 12, v2
	v_add_u32_e32 v13, v12, v11
	s_addc_u32 s43, s5, 0
	v_lshrrev_b32_e32 v7, 12, v4
	v_cndmask_b32_e32 v13, 0, v13, vcc
	v_addc_co_u32_e64 v11, s[40:41], v12, v11, vcc
	s_bcnt1_i32_b64 s5, vcc
	v_cmp_eq_u32_e32 vcc, 1, v6
	v_cndmask_b32_e64 v11, 0, v11, s[38:39]
	s_bcnt1_i32_b64 s30, s[38:39]
	v_cmp_eq_u32_e64 s[38:39], 1, v7
	v_mbcnt_lo_u32_b32 v12, vcc_lo, 0
	s_add_i32 s5, s30, s5
	v_mbcnt_hi_u32_b32 v12, vcc_hi, v12
	v_mbcnt_lo_u32_b32 v14, s38, 0
	v_mbcnt_hi_u32_b32 v14, s39, v14
	v_add_u32_e32 v12, s5, v12
	v_add_u32_e32 v15, v12, v14
	v_addc_co_u32_e64 v12, s[40:41], v12, v14, vcc
	s_bcnt1_i32_b64 s30, vcc
	v_cndmask_b32_e32 v13, v13, v15, vcc
	v_cndmask_b32_e64 v11, v11, v12, s[38:39]
	s_bcnt1_i32_b64 s38, s[38:39]
	s_add_i32 s30, s5, s30
	v_cmp_eq_u32_e32 vcc, 2, v6
	s_add_i32 s30, s30, s38
	v_cmp_eq_u32_e64 s[38:39], 2, v7
	v_mbcnt_lo_u32_b32 v12, vcc_lo, 0
	v_mbcnt_hi_u32_b32 v12, vcc_hi, v12
	v_mbcnt_lo_u32_b32 v14, s38, 0
	v_mbcnt_hi_u32_b32 v14, s39, v14
	v_add_u32_e32 v12, s30, v12
	v_add_u32_e32 v15, v12, v14
	v_addc_co_u32_e64 v12, s[40:41], v12, v14, vcc
	s_bcnt1_i32_b64 s40, vcc
	s_lshl_b32 s44, s30, 8
	v_cndmask_b32_e32 v13, v13, v15, vcc
	v_cndmask_b32_e64 v11, v11, v12, s[38:39]
	s_bcnt1_i32_b64 s38, s[38:39]
	s_add_i32 s30, s30, s40
	v_cmp_eq_u32_e32 vcc, 3, v6
	s_add_i32 s30, s30, s38
	v_cmp_eq_u32_e64 s[38:39], 3, v7
	v_mbcnt_lo_u32_b32 v6, vcc_lo, 0
	v_mbcnt_hi_u32_b32 v6, vcc_hi, v6
	v_mbcnt_lo_u32_b32 v7, s38, 0
	v_mbcnt_hi_u32_b32 v7, s39, v7
	v_add_u32_e32 v6, s30, v6
	v_add_u32_e32 v12, v6, v7
	v_cndmask_b32_e32 v12, v13, v12, vcc
	v_addc_co_u32_e32 v6, vcc, v6, v7, vcc
	v_cndmask_b32_e64 v6, v11, v6, s[38:39]
	v_lshl_add_u32 v7, v12, 3, s33
	ds_write_b64 v7, v[2:3]
	v_lshl_add_u32 v2, v6, 3, s33
	ds_write_b64 v2, v[4:5]
	ds_read_b128 v[2:5], v10
	s_lshl_b32 s30, s30, 16
	s_or_b32 s30, s44, s30
	v_lshl_add_u32 v247, v74, 2, s94
	s_or_b32 s5, s30, s5
	s_waitcnt lgkmcnt(0)
	v_and_b32_e32 v2, 0xffff, v2
	v_lshl_or_b32 v2, v4, 16, v2
	ds_write_b32 v247, v2 offset:3840
	v_mov_b32_e32 v2, s5
	v_cmp_eq_u32_e32 vcc, 15, v74
	v_lshlrev_b32_e32 v224, 4, v74
	v_mov_b32_e32 v4, v3
	v_cndmask_b32_e32 v248, v9, v2, vcc
	v_bfe_u32 v2, v74, 2, 2
	v_ashrrev_i32_e32 v225, 31, v224
	s_add_u32 s46, s18, 0x26400000
	ds_write_b64 v8, v[4:5] offset:7680
	v_cmp_eq_u32_e64 s[38:39], v2, v1
	v_lshl_add_u64 v[2:3], s[42:43], 0, v[224:225]
	s_mov_b64 s[40:41], 0xe00000
	v_and_b32_e32 v4, 2, v74
	s_addc_u32 s47, s19, 0
	s_waitcnt vmcnt(0) lgkmcnt(0)
	v_lshl_add_u64 v[140:141], v[2:3], 0, s[40:41]
	v_cmp_eq_u32_e64 s[40:41], 0, v4
	v_and_b32_e32 v4, 1, v74
	v_ashrrev_i32_e32 v5, 3, v74
	s_add_u32 s6, s46, s6
	v_cmp_eq_u32_e64 s[42:43], 0, v4
	v_lshlrev_b32_e32 v4, 1, v1
	v_and_b32_e32 v5, -4, v5
	s_addc_u32 s7, s47, s7
	s_mov_b32 s3, 0
	v_cmp_eq_u32_e64 s[44:45], 0, v150
	v_and_or_b32 v152, v4, 2, v5
	v_lshl_add_u64 v[142:143], s[6:7], 0, v[224:225]
	v_lshl_add_u64 v[144:145], s[46:47], 0, v[224:225]
	v_mov_b32_e32 v183, 1.0
	v_cndmask_b32_e64 v184, 0, v183, s[38:39]
	v_cndmask_b32_e64 v185, 0, v184, s[40:41]
	v_cndmask_b32_e64 v186, v184, 0, s[40:41]
	v_cndmask_b32_e64 v174, 0, v185, s[42:43]
	v_cndmask_b32_e64 v175, v185, 0, s[42:43]
	v_cndmask_b32_e64 v176, 0, v186, s[42:43]
	v_cndmask_b32_e64 v177, v186, 0, s[42:43]
	v_mov_b32_e32 v178, 0x39800000
	v_mov_b32_e32 v179, 0x3d372713
	v_mov_b32_e32 v180, 0x3fcc422a
	v_mov_b32_e32 v181, 0xbfb8aa3b
	v_mov_b32_e32 v182, 0x3c800000
	s_branch .LBB0_1729

.LBB0_1741:
	s_waitcnt vmcnt(15)
	v_mfma_f32_16x16x32_fp8_fp8 v[164:167], v[72:73], v[148:149], 0
	v_mfma_f32_16x16x32_fp8_fp8 v[164:167], v[74:75], v[146:147], v[164:167]
	s_lshl_b32 s30, s58, 9
	v_lshl_add_u32 v136, s48, 4, v152
	s_add_i32 s30, s15, s30
	s_waitcnt vmcnt(14)
	v_mfma_f32_16x16x32_fp8_fp8 v[154:157], v[76:77], v[148:149], 0
	v_mfma_f32_16x16x32_fp8_fp8 v[154:157], v[78:79], v[146:147], v[154:157]
	s_waitcnt vmcnt(13)
	v_mfma_f32_16x16x32_fp8_fp8 v[168:171], v[80:81], v[148:149], 0
	v_mfma_f32_16x16x32_fp8_fp8 v[168:171], v[82:83], v[146:147], v[168:171]
	v_pk_mul_f32 v[172:173], v[164:165], v[174:175]
	v_pk_fma_f32 v[172:173], v[166:167], v[176:177], v[172:173]
	v_add_f32_e32 v137, v172, v173
	s_waitcnt vmcnt(12)
	v_mfma_f32_16x16x32_fp8_fp8 v[164:167], v[84:85], v[148:149], 0
	v_mfma_f32_16x16x32_fp8_fp8 v[164:167], v[86:87], v[146:147], v[164:167]
	v_pk_mul_f32 v[172:173], v[154:155], v[174:175]
	v_pk_fma_f32 v[172:173], v[156:157], v[176:177], v[172:173]
	v_add_f32_e32 v138, v172, v173
	s_waitcnt vmcnt(11)
	v_mfma_f32_16x16x32_fp8_fp8 v[154:157], v[88:89], v[148:149], 0
	v_mfma_f32_16x16x32_fp8_fp8 v[154:157], v[90:91], v[146:147], v[154:157]
	v_pk_mul_f32 v[172:173], v[168:169], v[174:175]
	v_pk_fma_f32 v[172:173], v[170:171], v[176:177], v[172:173]
	v_add_f32_e32 v139, v172, v173
	s_waitcnt vmcnt(10)
	v_mfma_f32_16x16x32_fp8_fp8 v[168:171], v[92:93], v[148:149], 0
	v_mfma_f32_16x16x32_fp8_fp8 v[168:171], v[94:95], v[146:147], v[168:171]
	v_pk_mul_f32 v[172:173], v[164:165], v[174:175]
	v_pk_fma_f32 v[172:173], v[166:167], v[176:177], v[172:173]
	v_add_f32_e32 v158, v172, v173
	s_waitcnt vmcnt(9)
	v_mfma_f32_16x16x32_fp8_fp8 v[164:167], v[96:97], v[148:149], 0
	v_mfma_f32_16x16x32_fp8_fp8 v[164:167], v[98:99], v[146:147], v[164:167]
	v_pk_mul_f32 v[172:173], v[154:155], v[174:175]
	v_pk_fma_f32 v[172:173], v[156:157], v[176:177], v[172:173]
	v_add_f32_e32 v159, v172, v173
	s_waitcnt vmcnt(8)
	v_mfma_f32_16x16x32_fp8_fp8 v[154:157], v[100:101], v[148:149], 0
	v_mfma_f32_16x16x32_fp8_fp8 v[154:157], v[102:103], v[146:147], v[154:157]
	v_pk_mul_f32 v[172:173], v[168:169], v[174:175]
	v_pk_fma_f32 v[172:173], v[170:171], v[176:177], v[172:173]
	v_add_f32_e32 v160, v172, v173
	v_pk_mul_f32 v[172:173], v[164:165], v[174:175]
	v_pk_fma_f32 v[172:173], v[166:167], v[176:177], v[172:173]
	v_add_f32_e32 v161, v172, v173
	s_nop 1
	v_pk_mul_f32 v[172:173], v[154:155], v[174:175]
	v_pk_fma_f32 v[172:173], v[156:157], v[176:177], v[172:173]
	v_add_f32_e32 v162, v172, v173
	v_permlane32_swap_b32_e32 v137, v159
	v_add_f32_e32 v137, v137, v159
	v_permlane32_swap_b32_e32 v138, v160
	v_add_f32_e32 v138, v138, v160
	v_permlane32_swap_b32_e32 v139, v161
	v_add_f32_e32 v139, v139, v161
	v_permlane32_swap_b32_e32 v158, v162
	v_add_f32_e32 v158, v158, v162
	v_permlane16_swap_b32_e32 v137, v139
	v_add_f32_e32 v137, v137, v139
	v_permlane16_swap_b32_e32 v138, v158
	v_add_f32_e32 v138, v138, v158
	v_add_f32_dpp v137, v137, v137 row_ror:8 row_mask:0xf bank_mask:0xf bound_ctrl:1
	s_nop 0
	v_add_f32_dpp v138, v138, v138 row_ror:8 row_mask:0xf bank_mask:0xf bound_ctrl:1
	v_add_f32_dpp v137, v137, v137 row_ror:4 row_mask:0xf bank_mask:0xf bound_ctrl:1
	s_nop 0
	v_add_f32_dpp v138, v138, v138 row_ror:4 row_mask:0xf bank_mask:0xf bound_ctrl:1
	v_add_f32_dpp v137, v137, v137 row_ror:2 row_mask:0xf bank_mask:0xf bound_ctrl:1
	s_nop 0
	v_add_f32_dpp v138, v138, v138 row_ror:2 row_mask:0xf bank_mask:0xf bound_ctrl:1
	v_add_f32_dpp v172, v137, v137 row_ror:1 row_mask:0xf bank_mask:0xf bound_ctrl:1
	s_nop 0
	v_add_f32_dpp v173, v138, v138 row_ror:1 row_mask:0xf bank_mask:0xf bound_ctrl:1
	v_lshl_add_u32 v137, v136, 2, s30
	s_lshl_b32 s72, s48, 4
	s_cmp_ge_i32 s72, s70
	s_cselect_b32 s73, 1, 0
	s_cmp_lt_i32 s72, s61
	s_cselect_b32 s72, 1, 0
	s_and_b32 s72, s72, s73
	s_cbranch_scc0 .Lug_h1g0_skip
	s_and_saveexec_b64 s[56:57], s[44:45]
	ds_read_b64 v[160:161], v137
	v_pk_mul_f32 v[172:173], v[172:173], v[178:179] op_sel_hi:[1,0]
	v_pk_mul_f32 v[158:159], v[172:173], v[178:179] op_sel:[0,1] op_sel_hi:[1,1]
	v_pk_mul_f32 v[158:159], v[172:173], v[158:159]
	v_pk_fma_f32 v[158:159], v[172:173], v[158:159], v[172:173]
	v_pk_mul_f32 v[158:159], v[158:159], v[180:181] op_sel_hi:[1,0]
	v_pk_mul_f32 v[158:159], v[158:159], v[180:181] op_sel:[0,1] op_sel_hi:[1,1]
	v_exp_f32_e32 v158, v158
	v_exp_f32_e32 v159, v159
	s_nop 0
	v_pk_add_f32 v[158:159], v[158:159], v[182:183] op_sel:[0,1] op_sel_hi:[1,1]
	v_rcp_f32_e32 v158, v158
	v_rcp_f32_e32 v159, v159
	s_nop 0
	v_pk_mul_f32 v[172:173], v[172:173], v[158:159]
	v_pk_mul_f32 v[172:173], v[172:173], v[182:183] op_sel_hi:[1,0]
	s_waitcnt lgkmcnt(0)
	v_pk_mul_f32 v[172:173], v[172:173], v[160:161]
	ds_write_b64 v137, v[172:173]
	s_or_b64 exec, exec, s[56:57]
; #define PL_LOAD(RB, TAB, SE, BB) do { _Pragma("unroll") for (int _q = 0; _q < 16; ++_q) { \
;         const unsigned _pw = (unsigned)__builtin_amdgcn_readlane((int)(SE), (BB) * 8 + (_q >> 1)); const unsigned _idx = (_q & 1) ? (_pw >> 16) : (_pw & 0xffffu); \
;         (RB)[_q] = *(const v4u*)((TAB) + (size_t)_idx * 1024 + 16 * lane); } } while (0)
; #define U_ADV() do { ++lb; if (lb >= lbh) { ++lt; if (lt < 16) { U_RANGE(lt, ps, _r0, _r1, _b0, _b1); lb = _b0; lbh = _b1; (void)_r0; (void)_r1; seL = sIdx[lt * 64 + lane]; } } } while (0)
; #define U_SETC() do { ct = lt; cb = lb; { U_RANGE(ct, ps, _r0, _r1, _b0, _b1); crl = _r0; crh = _r1; cbl = _b0; (void)_b1; } } while (0)
; __device__ __forceinline__ void peer_unit(Frame& F, const Args& a, int layer, int unit, bool last) {
;     ...
;         PL_LOAD(ra, U8, seL, lb);
;         U_SETC(); U_ADV();
;         for (;;) {
;             if (lt < 16) PL_LOAD(rb, U8, seL, lb);
;             U_COMPUTE(ra);
;             if (lt >= 16) break;
;             U_SETC(); U_ADV();
.Lug_h1g0_skip:
	s_waitcnt vmcnt(7)
	v_mfma_f32_16x16x32_fp8_fp8 v[164:167], v[104:105], v[148:149], 0
	v_mfma_f32_16x16x32_fp8_fp8 v[164:167], v[106:107], v[146:147], v[164:167]
	s_waitcnt vmcnt(6)
	v_mfma_f32_16x16x32_fp8_fp8 v[154:157], v[108:109], v[148:149], 0
	v_mfma_f32_16x16x32_fp8_fp8 v[154:157], v[110:111], v[146:147], v[154:157]
	s_waitcnt vmcnt(5)
	v_mfma_f32_16x16x32_fp8_fp8 v[168:171], v[112:113], v[148:149], 0
	v_mfma_f32_16x16x32_fp8_fp8 v[168:171], v[114:115], v[146:147], v[168:171]
	s_nop 1
	v_pk_mul_f32 v[172:173], v[164:165], v[174:175]
	v_pk_fma_f32 v[172:173], v[166:167], v[176:177], v[172:173]
	v_add_f32_e32 v138, v172, v173
	s_waitcnt vmcnt(4)
	v_mfma_f32_16x16x32_fp8_fp8 v[164:167], v[116:117], v[148:149], 0
	v_mfma_f32_16x16x32_fp8_fp8 v[164:167], v[118:119], v[146:147], v[164:167]
	v_pk_mul_f32 v[172:173], v[154:155], v[174:175]
	v_pk_fma_f32 v[172:173], v[156:157], v[176:177], v[172:173]
	v_add_f32_e32 v139, v172, v173
	s_waitcnt vmcnt(3)
	v_mfma_f32_16x16x32_fp8_fp8 v[154:157], v[120:121], v[148:149], 0
	v_mfma_f32_16x16x32_fp8_fp8 v[154:157], v[122:123], v[146:147], v[154:157]
	v_pk_mul_f32 v[172:173], v[168:169], v[174:175]
	v_pk_fma_f32 v[172:173], v[170:171], v[176:177], v[172:173]
	v_add_f32_e32 v158, v172, v173
	s_waitcnt vmcnt(2)
	v_mfma_f32_16x16x32_fp8_fp8 v[168:171], v[124:125], v[148:149], 0
	v_mfma_f32_16x16x32_fp8_fp8 v[168:171], v[126:127], v[146:147], v[168:171]
	v_pk_mul_f32 v[172:173], v[164:165], v[174:175]
	v_pk_fma_f32 v[172:173], v[166:167], v[176:177], v[172:173]
	v_add_f32_e32 v159, v172, v173
	s_waitcnt vmcnt(1)
	v_mfma_f32_16x16x32_fp8_fp8 v[164:167], v[128:129], v[148:149], 0
	v_mfma_f32_16x16x32_fp8_fp8 v[164:167], v[130:131], v[146:147], v[164:167]
	v_pk_mul_f32 v[172:173], v[154:155], v[174:175]
	v_pk_fma_f32 v[172:173], v[156:157], v[176:177], v[172:173]
	v_add_f32_e32 v160, v172, v173
	s_waitcnt vmcnt(0)
	v_mfma_f32_16x16x32_fp8_fp8 v[154:157], v[132:133], v[148:149], 0
	v_mfma_f32_16x16x32_fp8_fp8 v[154:157], v[134:135], v[146:147], v[154:157]
	v_pk_mul_f32 v[172:173], v[168:169], v[174:175]
	v_pk_fma_f32 v[172:173], v[170:171], v[176:177], v[172:173]
	v_add_f32_e32 v161, v172, v173
	v_pk_mul_f32 v[172:173], v[164:165], v[174:175]
	v_pk_fma_f32 v[172:173], v[166:167], v[176:177], v[172:173]
	v_add_f32_e32 v162, v172, v173
	s_nop 1
	v_pk_mul_f32 v[172:173], v[154:155], v[174:175]
	v_pk_fma_f32 v[172:173], v[156:157], v[176:177], v[172:173]
	v_add_f32_e32 v163, v172, v173
	v_permlane32_swap_b32_e32 v138, v160
	v_add_f32_e32 v138, v138, v160
	v_permlane32_swap_b32_e32 v139, v161
	v_add_f32_e32 v139, v139, v161
	v_permlane32_swap_b32_e32 v158, v162
	v_add_f32_e32 v158, v158, v162
	v_permlane32_swap_b32_e32 v159, v163
	v_add_f32_e32 v159, v159, v163
	v_permlane16_swap_b32_e32 v138, v158
	v_add_f32_e32 v138, v138, v158
	v_permlane16_swap_b32_e32 v139, v159
	v_add_f32_e32 v139, v139, v159
	v_add_f32_dpp v138, v138, v138 row_ror:8 row_mask:0xf bank_mask:0xf bound_ctrl:1
	s_nop 0
	v_add_f32_dpp v139, v139, v139 row_ror:8 row_mask:0xf bank_mask:0xf bound_ctrl:1
	v_add_f32_dpp v138, v138, v138 row_ror:4 row_mask:0xf bank_mask:0xf bound_ctrl:1
	s_nop 0
	v_add_f32_dpp v139, v139, v139 row_ror:4 row_mask:0xf bank_mask:0xf bound_ctrl:1
	v_add_f32_dpp v138, v138, v138 row_ror:2 row_mask:0xf bank_mask:0xf bound_ctrl:1
	s_nop 0
	v_add_f32_dpp v139, v139, v139 row_ror:2 row_mask:0xf bank_mask:0xf bound_ctrl:1
	v_add_f32_dpp v172, v138, v138 row_ror:1 row_mask:0xf bank_mask:0xf bound_ctrl:1
	s_nop 0
	v_add_f32_dpp v173, v139, v139 row_ror:1 row_mask:0xf bank_mask:0xf bound_ctrl:1
	s_lshl_b32 s72, s48, 4
	s_cmp_ge_i32 s72, s70
	s_cselect_b32 s73, 1, 0
	s_cmp_lt_i32 s72, s61
	s_cselect_b32 s72, 1, 0
	s_and_b32 s72, s72, s73
	s_cbranch_scc0 .Lug_h1g1_skip
	s_and_saveexec_b64 s[56:57], s[44:45]
	ds_read_b64 v[160:161], v137 offset:32
	v_pk_mul_f32 v[172:173], v[172:173], v[178:179] op_sel_hi:[1,0]
	v_pk_mul_f32 v[158:159], v[172:173], v[178:179] op_sel:[0,1] op_sel_hi:[1,1]
	v_pk_mul_f32 v[158:159], v[172:173], v[158:159]
	v_pk_fma_f32 v[158:159], v[172:173], v[158:159], v[172:173]
	v_pk_mul_f32 v[158:159], v[158:159], v[180:181] op_sel_hi:[1,0]
	v_pk_mul_f32 v[158:159], v[158:159], v[180:181] op_sel:[0,1] op_sel_hi:[1,1]
	v_exp_f32_e32 v158, v158
	v_exp_f32_e32 v159, v159
	s_nop 0
	v_pk_add_f32 v[158:159], v[158:159], v[182:183] op_sel:[0,1] op_sel_hi:[1,1]
	v_rcp_f32_e32 v158, v158
	v_rcp_f32_e32 v159, v159
	s_nop 0
	v_pk_mul_f32 v[172:173], v[172:173], v[158:159]
	v_pk_mul_f32 v[172:173], v[172:173], v[182:183] op_sel_hi:[1,0]
	s_waitcnt lgkmcnt(0)
	v_pk_mul_f32 v[172:173], v[172:173], v[160:161]
	ds_write_b64 v137, v[172:173] offset:32
	s_or_b64 exec, exec, s[56:57]
.Lug_h1g1_skip:
	s_cmp_gt_i32 s59, 15
	s_cbranch_scc1 .LBB0_1733
	s_add_i32 s48, s60, 1
	s_cmp_lt_i32 s48, s5
	v_readlane_b32 s46, v248, s59
	s_cbranch_scc1 .LBB0_1755
	s_cmp_eq_u32 s59, 15
	s_mov_b32 s58, 16
	s_cbranch_scc1 .LBB0_1756
	s_add_i32 s58, s59, 1
	v_readlane_b32 s5, v248, s58
	s_and_b32 s30, s5, 0xff
	s_bfe_u32 s47, s5, 0x80008
	s_bfe_u32 s5, s5, 0x80010
	s_add_i32 s30, s30, 15
	s_add_i32 s47, s47, 15
	s_add_i32 s5, s5, 15
	s_and_b32 s30, s30, 0x1f0
	s_and_b32 s47, s47, 0x1f0
	s_and_b32 s5, s5, 0x1f0
	s_min_u32 s30, s30, 0x80
	s_min_u32 s47, s47, 0x80
	s_min_u32 s5, s5, 0x80
	s_and_b64 s[56:57], s[6:7], exec
	s_cselect_b32 s48, s47, s5
	s_and_b64 s[56:57], s[52:53], exec
	s_cselect_b32 s48, s30, s48
	s_and_b64 s[56:57], s[6:7], exec
	s_cselect_b32 s5, s5, 0x80
	s_and_b64 s[56:57], s[52:53], exec
	s_cselect_b32 s5, s47, s5
	s_and_b64 s[56:57], s[54:55], exec
	s_cselect_b32 s5, s30, s5
	s_lshr_b32 s30, s48, 4
	v_lshl_add_u32 v136, s58, 8, v247
	s_min_u32 s30, s30, 7
	s_waitcnt lgkmcnt(0)
	ds_read_b32 v153, v136
	s_and_b64 s[56:57], s[54:55], exec
	s_cselect_b32 s48, 0, s30
	s_lshr_b32 s5, s5, 4
	s_add_i32 s30, s48, 1
	s_max_u32 s5, s5, s30
	s_branch .LBB0_1756

; #define PL_LOAD(RB, TAB, SE, BB) do { _Pragma("unroll") for (int _q = 0; _q < 16; ++_q) { \
;         const unsigned _pw = (unsigned)__builtin_amdgcn_readlane((int)(SE), (BB) * 8 + (_q >> 1)); const unsigned _idx = (_q & 1) ? (_pw >> 16) : (_pw & 0xffffu); \
;         (RB)[_q] = *(const v4u*)((TAB) + (size_t)_idx * 1024 + 16 * lane); } } while (0)
; #define U_ADV() do { ++lb; if (lb >= lbh) { ++lt; if (lt < 16) { U_RANGE(lt, ps, _r0, _r1, _b0, _b1); lb = _b0; lbh = _b1; (void)_r0; (void)_r1; seL = sIdx[lt * 64 + lane]; } } } while (0)
; #define U_SETC() do { ct = lt; cb = lb; { U_RANGE(ct, ps, _r0, _r1, _b0, _b1); crl = _r0; crh = _r1; cbl = _b0; (void)_b1; } } while (0)
; __device__ __forceinline__ void peer_unit(Frame& F, const Args& a, int layer, int unit, bool last) {
;     ...
;         PL_LOAD(ra, U8, seL, lb);
;         U_SETC(); U_ADV();
;         for (;;) {
;             if (lt < 16) PL_LOAD(rb, U8, seL, lb);
;             U_COMPUTE(ra);
;             if (lt >= 16) break;
;             U_SETC(); U_ADV();
;             if (lt < 16) PL_LOAD(ra, U8, seL, lb);
;             U_COMPUTE(rb);
.LBB0_1762:
	v_mfma_f32_16x16x32_fp8_fp8 v[164:167], v[4:5], v[148:149], 0
	v_mfma_f32_16x16x32_fp8_fp8 v[164:167], v[6:7], v[146:147], v[164:167]
	s_and_b64 s[70:71], s[6:7], exec
	s_cselect_b32 s46, s46, 0x80
	s_and_b64 s[70:71], s[52:53], exec
	s_cselect_b32 s46, s56, s46
	s_and_b64 s[56:57], s[54:55], exec
	s_cselect_b32 s61, s47, s46
	s_lshl_b32 s46, s59, 9
	v_lshl_add_u32 v136, s60, 4, v152
	s_add_i32 s46, s15, s46
	v_mfma_f32_16x16x32_fp8_fp8 v[154:157], v[8:9], v[148:149], 0
	v_mfma_f32_16x16x32_fp8_fp8 v[154:157], v[10:11], v[146:147], v[154:157]
	v_mfma_f32_16x16x32_fp8_fp8 v[168:171], v[12:13], v[148:149], 0
	v_mfma_f32_16x16x32_fp8_fp8 v[168:171], v[14:15], v[146:147], v[168:171]
	v_pk_mul_f32 v[172:173], v[164:165], v[174:175]
	v_pk_fma_f32 v[172:173], v[166:167], v[176:177], v[172:173]
	v_add_f32_e32 v137, v172, v173
	v_mfma_f32_16x16x32_fp8_fp8 v[164:167], v[16:17], v[148:149], 0
	v_mfma_f32_16x16x32_fp8_fp8 v[164:167], v[18:19], v[146:147], v[164:167]
	s_nop 0
	v_pk_mul_f32 v[172:173], v[154:155], v[174:175]
	v_pk_fma_f32 v[172:173], v[156:157], v[176:177], v[172:173]
	v_add_f32_e32 v138, v172, v173
	v_mfma_f32_16x16x32_fp8_fp8 v[154:157], v[20:21], v[148:149], 0
	v_mfma_f32_16x16x32_fp8_fp8 v[154:157], v[22:23], v[146:147], v[154:157]
	v_pk_mul_f32 v[172:173], v[168:169], v[174:175]
	v_pk_fma_f32 v[172:173], v[170:171], v[176:177], v[172:173]
	v_add_f32_e32 v139, v172, v173
	v_mfma_f32_16x16x32_fp8_fp8 v[168:171], v[24:25], v[148:149], 0
	v_mfma_f32_16x16x32_fp8_fp8 v[168:171], v[26:27], v[146:147], v[168:171]
	v_pk_mul_f32 v[172:173], v[164:165], v[174:175]
	v_pk_fma_f32 v[172:173], v[166:167], v[176:177], v[172:173]
	v_add_f32_e32 v158, v172, v173
	v_mfma_f32_16x16x32_fp8_fp8 v[164:167], v[28:29], v[148:149], 0
	v_mfma_f32_16x16x32_fp8_fp8 v[164:167], v[30:31], v[146:147], v[164:167]
	v_pk_mul_f32 v[172:173], v[154:155], v[174:175]
	v_pk_fma_f32 v[172:173], v[156:157], v[176:177], v[172:173]
	v_add_f32_e32 v159, v172, v173
	v_mfma_f32_16x16x32_fp8_fp8 v[154:157], v[32:33], v[148:149], 0
	v_mfma_f32_16x16x32_fp8_fp8 v[154:157], v[34:35], v[146:147], v[154:157]
	v_pk_mul_f32 v[172:173], v[168:169], v[174:175]
	v_pk_fma_f32 v[172:173], v[170:171], v[176:177], v[172:173]
	v_add_f32_e32 v160, v172, v173
	v_pk_mul_f32 v[172:173], v[164:165], v[174:175]
	v_pk_fma_f32 v[172:173], v[166:167], v[176:177], v[172:173]
	v_add_f32_e32 v161, v172, v173
	s_nop 1
	v_pk_mul_f32 v[172:173], v[154:155], v[174:175]
	v_pk_fma_f32 v[172:173], v[156:157], v[176:177], v[172:173]
	v_add_f32_e32 v162, v172, v173
	v_permlane32_swap_b32_e32 v137, v159
	v_add_f32_e32 v137, v137, v159
	v_permlane32_swap_b32_e32 v138, v160
	v_add_f32_e32 v138, v138, v160
	v_permlane32_swap_b32_e32 v139, v161
	v_add_f32_e32 v139, v139, v161
	v_permlane32_swap_b32_e32 v158, v162
	v_add_f32_e32 v158, v158, v162
	v_permlane16_swap_b32_e32 v137, v139
	v_add_f32_e32 v137, v137, v139
	v_permlane16_swap_b32_e32 v138, v158
	v_add_f32_e32 v138, v138, v158
	v_add_f32_dpp v137, v137, v137 row_ror:8 row_mask:0xf bank_mask:0xf bound_ctrl:1
	s_nop 0
	v_add_f32_dpp v138, v138, v138 row_ror:8 row_mask:0xf bank_mask:0xf bound_ctrl:1
	v_add_f32_dpp v137, v137, v137 row_ror:4 row_mask:0xf bank_mask:0xf bound_ctrl:1
	s_nop 0
	v_add_f32_dpp v138, v138, v138 row_ror:4 row_mask:0xf bank_mask:0xf bound_ctrl:1
	v_add_f32_dpp v137, v137, v137 row_ror:2 row_mask:0xf bank_mask:0xf bound_ctrl:1
	s_nop 0
	v_add_f32_dpp v138, v138, v138 row_ror:2 row_mask:0xf bank_mask:0xf bound_ctrl:1
	v_add_f32_dpp v172, v137, v137 row_ror:1 row_mask:0xf bank_mask:0xf bound_ctrl:1
	s_nop 0
	v_add_f32_dpp v173, v138, v138 row_ror:1 row_mask:0xf bank_mask:0xf bound_ctrl:1
	v_lshl_add_u32 v137, v136, 2, s46
	s_lshl_b32 s70, s60, 4
	s_cmp_ge_i32 s70, s30
	s_cselect_b32 s71, 1, 0
	s_cmp_lt_i32 s70, s61
	s_cselect_b32 s70, 1, 0
	s_and_b32 s70, s70, s71
	s_cbranch_scc0 .Lug_h2g0_skip
	s_and_saveexec_b64 s[56:57], s[44:45]
	ds_read_b64 v[160:161], v137
	v_pk_mul_f32 v[172:173], v[172:173], v[178:179] op_sel_hi:[1,0]
	v_pk_mul_f32 v[158:159], v[172:173], v[178:179] op_sel:[0,1] op_sel_hi:[1,1]
	v_pk_mul_f32 v[158:159], v[172:173], v[158:159]
	v_pk_fma_f32 v[158:159], v[172:173], v[158:159], v[172:173]
	v_pk_mul_f32 v[158:159], v[158:159], v[180:181] op_sel_hi:[1,0]
	v_pk_mul_f32 v[158:159], v[158:159], v[180:181] op_sel:[0,1] op_sel_hi:[1,1]
	v_exp_f32_e32 v158, v158
	v_exp_f32_e32 v159, v159
	s_nop 0
	v_pk_add_f32 v[158:159], v[158:159], v[182:183] op_sel:[0,1] op_sel_hi:[1,1]
	v_rcp_f32_e32 v158, v158
	v_rcp_f32_e32 v159, v159
	s_nop 0
	v_pk_mul_f32 v[172:173], v[172:173], v[158:159]
	v_pk_mul_f32 v[172:173], v[172:173], v[182:183] op_sel_hi:[1,0]
	s_waitcnt lgkmcnt(0)
	v_pk_mul_f32 v[172:173], v[172:173], v[160:161]
	ds_write_b64 v137, v[172:173]
	s_or_b64 exec, exec, s[56:57]
; #define PL_LOAD(RB, TAB, SE, BB) do { _Pragma("unroll") for (int _q = 0; _q < 16; ++_q) { \
;         const unsigned _pw = (unsigned)__builtin_amdgcn_readlane((int)(SE), (BB) * 8 + (_q >> 1)); const unsigned _idx = (_q & 1) ? (_pw >> 16) : (_pw & 0xffffu); \
;         (RB)[_q] = *(const v4u*)((TAB) + (size_t)_idx * 1024 + 16 * lane); } } while (0)
; #define U_ADV() do { ++lb; if (lb >= lbh) { ++lt; if (lt < 16) { U_RANGE(lt, ps, _r0, _r1, _b0, _b1); lb = _b0; lbh = _b1; (void)_r0; (void)_r1; seL = sIdx[lt * 64 + lane]; } } } while (0)
; #define U_SETC() do { ct = lt; cb = lb; { U_RANGE(ct, ps, _r0, _r1, _b0, _b1); crl = _r0; crh = _r1; cbl = _b0; (void)_b1; } } while (0)
; __device__ __forceinline__ void peer_unit(Frame& F, const Args& a, int layer, int unit, bool last) {
;     ...
;         PL_LOAD(ra, U8, seL, lb);
;         U_SETC(); U_ADV();
;         for (;;) {
;             if (lt < 16) PL_LOAD(rb, U8, seL, lb);
;             U_COMPUTE(ra);
;             if (lt >= 16) break;
;             U_SETC(); U_ADV();
;             if (lt < 16) PL_LOAD(ra, U8, seL, lb);
;             U_COMPUTE(rb);
;             if (lt >= 16) break;
;             U_SETC(); U_ADV();
.Lug_h2g0_skip:
	v_mfma_f32_16x16x32_fp8_fp8 v[164:167], v[36:37], v[148:149], 0
	v_mfma_f32_16x16x32_fp8_fp8 v[164:167], v[38:39], v[146:147], v[164:167]
	v_mfma_f32_16x16x32_fp8_fp8 v[154:157], v[40:41], v[148:149], 0
	v_mfma_f32_16x16x32_fp8_fp8 v[154:157], v[42:43], v[146:147], v[154:157]
	v_mfma_f32_16x16x32_fp8_fp8 v[168:171], v[44:45], v[148:149], 0
	v_mfma_f32_16x16x32_fp8_fp8 v[168:171], v[46:47], v[146:147], v[168:171]
	s_nop 3
	v_pk_mul_f32 v[172:173], v[164:165], v[174:175]
	v_pk_fma_f32 v[172:173], v[166:167], v[176:177], v[172:173]
	v_add_f32_e32 v138, v172, v173
	v_mfma_f32_16x16x32_fp8_fp8 v[164:167], v[48:49], v[148:149], 0
	v_mfma_f32_16x16x32_fp8_fp8 v[164:167], v[50:51], v[146:147], v[164:167]
	v_pk_mul_f32 v[172:173], v[154:155], v[174:175]
	v_pk_fma_f32 v[172:173], v[156:157], v[176:177], v[172:173]
	v_add_f32_e32 v139, v172, v173
	v_mfma_f32_16x16x32_fp8_fp8 v[154:157], v[52:53], v[148:149], 0
	v_mfma_f32_16x16x32_fp8_fp8 v[154:157], v[54:55], v[146:147], v[154:157]
	v_pk_mul_f32 v[172:173], v[168:169], v[174:175]
	v_pk_fma_f32 v[172:173], v[170:171], v[176:177], v[172:173]
	v_add_f32_e32 v158, v172, v173
	v_mfma_f32_16x16x32_fp8_fp8 v[168:171], v[56:57], v[148:149], 0
	v_mfma_f32_16x16x32_fp8_fp8 v[168:171], v[58:59], v[146:147], v[168:171]
	v_pk_mul_f32 v[172:173], v[164:165], v[174:175]
	v_pk_fma_f32 v[172:173], v[166:167], v[176:177], v[172:173]
	v_add_f32_e32 v159, v172, v173
	v_mfma_f32_16x16x32_fp8_fp8 v[164:167], v[60:61], v[148:149], 0
	v_mfma_f32_16x16x32_fp8_fp8 v[164:167], v[62:63], v[146:147], v[164:167]
	v_pk_mul_f32 v[172:173], v[154:155], v[174:175]
	v_pk_fma_f32 v[172:173], v[156:157], v[176:177], v[172:173]
	v_add_f32_e32 v160, v172, v173
	v_mfma_f32_16x16x32_fp8_fp8 v[154:157], v[64:65], v[148:149], 0
	v_mfma_f32_16x16x32_fp8_fp8 v[154:157], v[66:67], v[146:147], v[154:157]
	v_pk_mul_f32 v[172:173], v[168:169], v[174:175]
	v_pk_fma_f32 v[172:173], v[170:171], v[176:177], v[172:173]
	v_add_f32_e32 v161, v172, v173
	v_pk_mul_f32 v[172:173], v[164:165], v[174:175]
	v_pk_fma_f32 v[172:173], v[166:167], v[176:177], v[172:173]
	v_add_f32_e32 v162, v172, v173
	s_nop 1
	v_pk_mul_f32 v[172:173], v[154:155], v[174:175]
	v_pk_fma_f32 v[172:173], v[156:157], v[176:177], v[172:173]
	v_add_f32_e32 v163, v172, v173
	v_permlane32_swap_b32_e32 v138, v160
	v_add_f32_e32 v138, v138, v160
	v_permlane32_swap_b32_e32 v139, v161
	v_add_f32_e32 v139, v139, v161
	v_permlane32_swap_b32_e32 v158, v162
	v_add_f32_e32 v158, v158, v162
	v_permlane32_swap_b32_e32 v159, v163
	v_add_f32_e32 v159, v159, v163
	v_permlane16_swap_b32_e32 v138, v158
	v_add_f32_e32 v138, v138, v158
	v_permlane16_swap_b32_e32 v139, v159
	v_add_f32_e32 v139, v139, v159
	v_add_f32_dpp v138, v138, v138 row_ror:8 row_mask:0xf bank_mask:0xf bound_ctrl:1
	s_nop 0
	v_add_f32_dpp v139, v139, v139 row_ror:8 row_mask:0xf bank_mask:0xf bound_ctrl:1
	v_add_f32_dpp v138, v138, v138 row_ror:4 row_mask:0xf bank_mask:0xf bound_ctrl:1
	s_nop 0
	v_add_f32_dpp v139, v139, v139 row_ror:4 row_mask:0xf bank_mask:0xf bound_ctrl:1
	v_add_f32_dpp v138, v138, v138 row_ror:2 row_mask:0xf bank_mask:0xf bound_ctrl:1
	s_nop 0
	v_add_f32_dpp v139, v139, v139 row_ror:2 row_mask:0xf bank_mask:0xf bound_ctrl:1
	v_add_f32_dpp v172, v138, v138 row_ror:1 row_mask:0xf bank_mask:0xf bound_ctrl:1
	s_nop 0
	v_add_f32_dpp v173, v139, v139 row_ror:1 row_mask:0xf bank_mask:0xf bound_ctrl:1
	s_lshl_b32 s70, s60, 4
	s_cmp_ge_i32 s70, s30
	s_cselect_b32 s71, 1, 0
	s_cmp_lt_i32 s70, s61
	s_cselect_b32 s70, 1, 0
	s_and_b32 s70, s70, s71
	s_cbranch_scc0 .Lug_h2g1_skip
	s_and_saveexec_b64 s[56:57], s[44:45]
	ds_read_b64 v[160:161], v137 offset:32
	v_pk_mul_f32 v[172:173], v[172:173], v[178:179] op_sel_hi:[1,0]
	v_pk_mul_f32 v[158:159], v[172:173], v[178:179] op_sel:[0,1] op_sel_hi:[1,1]
	v_pk_mul_f32 v[158:159], v[172:173], v[158:159]
	v_pk_fma_f32 v[158:159], v[172:173], v[158:159], v[172:173]
	v_pk_mul_f32 v[158:159], v[158:159], v[180:181] op_sel_hi:[1,0]
	v_pk_mul_f32 v[158:159], v[158:159], v[180:181] op_sel:[0,1] op_sel_hi:[1,1]
	v_exp_f32_e32 v158, v158
	v_exp_f32_e32 v159, v159
	s_nop 0
	v_pk_add_f32 v[158:159], v[158:159], v[182:183] op_sel:[0,1] op_sel_hi:[1,1]
	v_rcp_f32_e32 v158, v158
	v_rcp_f32_e32 v159, v159
	s_nop 0
	v_pk_mul_f32 v[172:173], v[172:173], v[158:159]
	v_pk_mul_f32 v[172:173], v[172:173], v[182:183] op_sel_hi:[1,0]
	s_waitcnt lgkmcnt(0)
	v_pk_mul_f32 v[172:173], v[172:173], v[160:161]
	ds_write_b64 v137, v[172:173] offset:32
	s_or_b64 exec, exec, s[56:57]
.Lug_h2g1_skip:
	s_cmp_gt_i32 s58, 15
	s_cbranch_scc1 .LBB0_1776
	v_readlane_b32 s30, v248, s58
	s_and_b32 s46, s30, 0xff
	s_add_i32 s46, s46, 15
	s_and_b32 s46, s46, 0x1f0
	s_min_u32 s56, s46, 0x80
	s_bfe_u32 s46, s30, 0x80008
	s_bfe_u32 s30, s30, 0x80010
	s_add_i32 s46, s46, 15
	s_add_i32 s30, s30, 15
	s_and_b32 s46, s46, 0x1f0
	s_and_b32 s30, s30, 0x1f0
	s_min_u32 s57, s46, 0x80
	s_min_u32 s30, s30, 0x80
	s_and_b64 s[46:47], s[6:7], exec
	s_cselect_b32 s59, s57, s30
	s_and_b64 s[46:47], s[52:53], exec
	s_cselect_b32 s59, s56, s59
	s_and_b64 s[46:47], s[54:55], exec
	s_cselect_b32 s70, 0, s59
	s_and_b64 s[46:47], s[6:7], exec
	s_cselect_b32 s30, s30, 0x80
	s_and_b64 s[46:47], s[52:53], exec
	s_cselect_b32 s30, s57, s30
	s_and_b64 s[46:47], s[54:55], exec
	s_cselect_b32 s61, s56, s30
	s_add_i32 s60, s48, 1
	s_cmp_lt_i32 s60, s5
	s_cbranch_scc1 .LBB0_1777
	s_cmp_eq_u32 s58, 15
	s_mov_b32 s59, 16
	s_cbranch_scc1 .LBB0_1778
	s_add_i32 s59, s58, 1
	v_readlane_b32 s5, v248, s59
	s_and_b32 s30, s5, 0xff
	s_bfe_u32 s46, s5, 0x80008
	s_bfe_u32 s5, s5, 0x80010
	s_add_i32 s30, s30, 15
	s_add_i32 s46, s46, 15
	s_add_i32 s5, s5, 15
	s_and_b32 s30, s30, 0x1f0
	s_and_b32 s46, s46, 0x1f0
	s_and_b32 s5, s5, 0x1f0
	s_min_u32 s30, s30, 0x80
	s_min_u32 s56, s46, 0x80
	s_min_u32 s5, s5, 0x80
	s_and_b64 s[46:47], s[6:7], exec
	s_cselect_b32 s57, s56, s5
	s_and_b64 s[46:47], s[52:53], exec
	s_cselect_b32 s57, s30, s57
	s_and_b64 s[46:47], s[6:7], exec
	s_cselect_b32 s5, s5, 0x80
	s_and_b64 s[46:47], s[52:53], exec
	s_cselect_b32 s5, s56, s5
	s_and_b64 s[46:47], s[54:55], exec
	s_cselect_b32 s5, s30, s5
	s_lshr_b32 s30, s57, 4
	v_lshl_add_u32 v136, s59, 8, v247
	s_min_u32 s30, s30, 7
	s_waitcnt lgkmcnt(0)
	ds_read_b32 v153, v136
	s_and_b64 s[46:47], s[54:55], exec
	s_cselect_b32 s60, 0, s30
	s_lshr_b32 s5, s5, 4
	s_add_i32 s30, s60, 1
	s_max_u32 s5, s5, s30
	s_branch .LBB0_1778

; #define PL_LOAD(RB, TAB, SE, BB) do { _Pragma("unroll") for (int _q = 0; _q < 16; ++_q) { \
;         const unsigned _pw = (unsigned)__builtin_amdgcn_readlane((int)(SE), (BB) * 8 + (_q >> 1)); const unsigned _idx = (_q & 1) ? (_pw >> 16) : (_pw & 0xffffu); \
;         (RB)[_q] = *(const v4u*)((TAB) + (size_t)_idx * 1024 + 16 * lane); } } while (0)
; #define V_ADV() do { ++lb; if (lb >= lbh) { ++lt; if (lt < 16) { V_RANGE(lt, ps, _r0, _r1, _b0, _b1); lb = _b0; lbh = _b1; (void)_r0; (void)_r1; seL = sIdx[lt * 64 + lane]; } } } while (0)
; #define V_SETC() do { ct = lt; cb = lb; { V_RANGE(ct, ps, _r0, _r1, _b0, _b1); crl = _r0; crh = _r1; cbl = _b0; cbh = _b1; } } while (0)
; __device__ __forceinline__ void peer_unit(Frame& F, const Args& a, int layer, int unit, bool last) {
;     ...
;         for (;;) {
;             if (lt < 16) PL_LOAD(rb, V8, seL, lb);
;             V_COMPUTE(ra);
;             if (lt >= 16) break;
;             V_SETC(); V_ADV();
;             if (lt < 16) PL_LOAD(ra, V8, seL, lb);
;             V_COMPUTE(rb);
.LBB0_1798:
	s_cmp_gt_i32 s57, 15
	s_cbranch_scc1 .Lpv_mid_nopf
	s_lshl_b32 s38, s59, 3
	s_waitcnt lgkmcnt(0)
	v_readlane_b32 s39, v250, s38
	s_lshl_b32 s30, s39, 10
	s_and_b32 s30, s30, 0x3fffc00
	v_lshl_add_u64 v[2:3], v[226:227], 0, s[30:31]
	s_bfe_u32 s30, s39, 0x100010
	s_lshl_b32 s30, s30, 10
	v_lshl_add_u64 v[8:9], v[226:227], 0, s[30:31]
	s_or_b32 s30, s38, 1
	v_readlane_b32 s39, v250, s30
	s_lshl_b32 s30, s39, 10
	s_and_b32 s30, s30, 0x3fffc00
	global_load_dwordx4 v[4:7], v[2:3], off
	s_nop 0
	global_load_dwordx4 v[8:11], v[8:9], off
	v_lshl_add_u64 v[2:3], v[226:227], 0, s[30:31]
	s_bfe_u32 s30, s39, 0x100010
	s_lshl_b32 s30, s30, 10
	v_lshl_add_u64 v[16:17], v[226:227], 0, s[30:31]
	s_or_b32 s30, s38, 2
	v_readlane_b32 s39, v250, s30
	s_lshl_b32 s30, s39, 10
	s_and_b32 s30, s30, 0x3fffc00
	global_load_dwordx4 v[12:15], v[2:3], off
	s_nop 0
	global_load_dwordx4 v[16:19], v[16:17], off
	v_lshl_add_u64 v[2:3], v[226:227], 0, s[30:31]
	s_bfe_u32 s30, s39, 0x100010
	s_lshl_b32 s30, s30, 10
	v_lshl_add_u64 v[24:25], v[226:227], 0, s[30:31]
	s_or_b32 s30, s38, 3
	v_readlane_b32 s39, v250, s30
	s_lshl_b32 s30, s39, 10
	s_and_b32 s30, s30, 0x3fffc00
	global_load_dwordx4 v[20:23], v[2:3], off
	s_nop 0
	global_load_dwordx4 v[24:27], v[24:25], off
	v_lshl_add_u64 v[2:3], v[226:227], 0, s[30:31]
	s_bfe_u32 s30, s39, 0x100010
	s_lshl_b32 s30, s30, 10
	v_lshl_add_u64 v[32:33], v[226:227], 0, s[30:31]
	s_or_b32 s30, s38, 4
	v_readlane_b32 s39, v250, s30
	s_lshl_b32 s30, s39, 10
	s_and_b32 s30, s30, 0x3fffc00
	global_load_dwordx4 v[28:31], v[2:3], off
	s_nop 0
	global_load_dwordx4 v[32:35], v[32:33], off
	v_lshl_add_u64 v[2:3], v[226:227], 0, s[30:31]
	s_bfe_u32 s30, s39, 0x100010
	s_lshl_b32 s30, s30, 10
	v_lshl_add_u64 v[40:41], v[226:227], 0, s[30:31]
	s_or_b32 s30, s38, 5
	v_readlane_b32 s39, v250, s30
	s_lshl_b32 s30, s39, 10
	s_and_b32 s30, s30, 0x3fffc00
	global_load_dwordx4 v[36:39], v[2:3], off
	s_nop 0
	global_load_dwordx4 v[40:43], v[40:41], off
	v_lshl_add_u64 v[2:3], v[226:227], 0, s[30:31]
	s_bfe_u32 s30, s39, 0x100010
	s_lshl_b32 s30, s30, 10
	v_lshl_add_u64 v[48:49], v[226:227], 0, s[30:31]
	s_or_b32 s30, s38, 6
	v_readlane_b32 s39, v250, s30
	s_lshl_b32 s30, s39, 10
	s_and_b32 s30, s30, 0x3fffc00
	global_load_dwordx4 v[44:47], v[2:3], off
	s_nop 0
	global_load_dwordx4 v[48:51], v[48:49], off
	v_lshl_add_u64 v[2:3], v[226:227], 0, s[30:31]
	s_bfe_u32 s30, s39, 0x100010
	s_lshl_b32 s30, s30, 10
	v_lshl_add_u64 v[56:57], v[226:227], 0, s[30:31]
	s_or_b32 s30, s38, 7
	v_readlane_b32 s38, v250, s30
	s_lshl_b32 s30, s38, 10
	s_and_b32 s30, s30, 0x3fffc00
	global_load_dwordx4 v[52:55], v[2:3], off
	s_nop 0
	global_load_dwordx4 v[56:59], v[56:57], off
	v_lshl_add_u64 v[2:3], v[226:227], 0, s[30:31]
	s_bfe_u32 s30, s38, 0x100010
	s_lshl_b32 s30, s30, 10
	v_lshl_add_u64 v[64:65], v[226:227], 0, s[30:31]
	global_load_dwordx4 v[60:63], v[2:3], off
	s_nop 0
	global_load_dwordx4 v[64:67], v[64:65], off
	s_waitcnt vmcnt(16)
	s_branch .Lpv_mid_go

.Lpv_mid_go:
	v_mov_b64_e32 v[178:179], v[170:171]
	v_mov_b64_e32 v[182:183], v[174:175]
	v_mov_b64_e32 v[176:177], v[168:169]
	v_mov_b64_e32 v[180:181], v[172:173]
	s_lshl_b32 s38, s58, 9
	s_add_i32 s38, s15, s38
	s_lshl_b32 s39, s56, 6
	s_add_i32 s38, s38, s39
	v_mov_b32_e32 v168, s38
	ds_read_b128 v[170:173], v168
	s_branch .Lpv_skip1
